# baseline (speedup 1.0000x reference)
.Lk4_st6_8:
	s_add_u32 s52, s10, 0x800000
	s_addc_u32 s53, s11, 0
	v_lshlrev_b32_e32 v169, 2, v94
	v_readfirstlane_b32 s14, v118
	s_mov_b32 m0, s14
	s_nop 0
	global_load_lds_dwordx4 v169, s[52:53] nt
	v_lshlrev_b32_e32 v169, 2, v96
	v_readfirstlane_b32 s14, v90
	s_mov_b32 m0, s14
	s_nop 0
	global_load_lds_dwordx4 v169, s[52:53] nt
	s_add_u32 s52, s10, 0xc00000
	s_addc_u32 s53, s11, 0
	v_lshlrev_b32_e32 v169, 2, v98
	v_lshlrev_b32_e32 v170, 2, v100
	global_load_dwordx4 v[140:143], v169, s[52:53] nt
	global_load_dwordx4 v[144:147], v170, s[52:53] nt
	s_add_u32 s52, s10, 0x1000000
	s_addc_u32 s53, s11, 0
	v_lshlrev_b32_e32 v169, 2, v94
	v_lshlrev_b32_e32 v170, 2, v96
	global_load_dwordx4 v[148:151], v169, s[52:53] nt
	global_load_dwordx4 v[152:155], v170, s[52:53] nt
	v_mfma_f32_16x16x32_f16 a[0:3], v[70:73], v[82:85], a[0:3]
	ds_read_b128 v[14:17], v158
	v_mfma_f32_16x16x32_f16 a[4:7], v[70:73], v[86:89], a[4:7]
	ds_read_b128 v[18:21], v160
	v_mfma_f32_16x16x32_f16 a[12:15], v[66:69], v[82:85], a[12:15]
	ds_read_b128 v[42:45], v168
	v_mfma_f32_16x16x32_f16 a[16:19], v[66:69], v[86:89], a[16:19]
	ds_read_b128 v[38:41], v168 offset:1024
	v_mfma_f32_16x16x32_f16 a[28:31], v[58:61], v[82:85], a[28:31]
	ds_read_b128 v[34:37], v168 offset:2048
	v_mfma_f32_16x16x32_f16 a[60:63], v[58:61], v[86:89], a[60:63]
	ds_read_b128 v[30:33], v168 offset:3072
	v_mfma_f32_16x16x32_f16 a[8:11], v[54:57], v[82:85], a[8:11]
	ds_read_b128 v[26:29], v168 offset:4096
	v_mfma_f32_16x16x32_f16 a[20:23], v[54:57], v[86:89], a[20:23]
	ds_read_b128 v[22:25], v168 offset:5120
	v_mfma_f32_16x16x32_f16 a[24:27], v[46:49], v[82:85], a[24:27]
	ds_read_b128 v[10:13], v168 offset:6144
	v_mfma_f32_16x16x32_f16 a[36:39], v[46:49], v[86:89], a[36:39]
	ds_read_b128 v[6:9], v168 offset:7168
	v_mfma_f32_16x16x32_f16 a[44:47], v[50:53], v[82:85], a[44:47]
	ds_read_b128 v[2:5], v168 offset:8192
	v_mfma_f32_16x16x32_f16 a[64:67], v[50:53], v[86:89], a[64:67]
	v_mfma_f32_16x16x32_f16 a[32:35], v[62:65], v[82:85], a[32:35]
	v_mfma_f32_16x16x32_f16 a[40:43], v[62:65], v[86:89], a[40:43]
	v_mfma_f32_16x16x32_f16 a[48:51], v[74:77], v[82:85], a[48:51]
	v_mfma_f32_16x16x32_f16 a[52:55], v[74:77], v[86:89], a[52:55]
	v_mfma_f32_16x16x32_f16 a[56:59], v[78:81], v[82:85], a[56:59]
	v_mfma_f32_16x16x32_f16 a[68:71], v[78:81], v[86:89], a[68:71]
	s_waitcnt lgkmcnt(8)
	v_mfma_f32_16x16x32_f16 a[0:3], v[42:45], v[14:17], a[0:3]
	ds_read_b128 v[82:85], v159
	v_mfma_f32_16x16x32_f16 a[4:7], v[42:45], v[18:21], a[4:7]
	ds_read_b128 v[86:89], v161
	s_waitcnt lgkmcnt(9)
	v_mfma_f32_16x16x32_f16 a[12:15], v[38:41], v[14:17], a[12:15]
	ds_read_b128 v[70:73], v168 offset:9216
	v_mfma_f32_16x16x32_f16 a[16:19], v[38:41], v[18:21], a[16:19]
	ds_read_b128 v[66:69], v168 offset:10240
	s_waitcnt lgkmcnt(10)
	v_mfma_f32_16x16x32_f16 a[28:31], v[34:37], v[14:17], a[28:31]
	ds_read_b128 v[58:61], v168 offset:11264
	v_mfma_f32_16x16x32_f16 a[60:63], v[34:37], v[18:21], a[60:63]
	ds_read_b128 v[54:57], v168 offset:12288
	s_waitcnt lgkmcnt(11)
	v_mfma_f32_16x16x32_f16 a[8:11], v[30:33], v[14:17], a[8:11]
	ds_read_b128 v[46:49], v168 offset:13312
	v_mfma_f32_16x16x32_f16 a[20:23], v[30:33], v[18:21], a[20:23]
	ds_read_b128 v[50:53], v168 offset:14336
	s_waitcnt lgkmcnt(12)
	v_mfma_f32_16x16x32_f16 a[24:27], v[26:29], v[14:17], a[24:27]
	ds_read_b128 v[62:65], v168 offset:15360
	v_mfma_f32_16x16x32_f16 a[36:39], v[26:29], v[18:21], a[36:39]
	ds_read_b128 v[74:77], v168 offset:16384
	s_waitcnt lgkmcnt(13)
	v_mfma_f32_16x16x32_f16 a[44:47], v[22:25], v[14:17], a[44:47]
	ds_read_b128 v[78:81], v168 offset:17408
	v_mfma_f32_16x16x32_f16 a[64:67], v[22:25], v[18:21], a[64:67]
	s_waitcnt lgkmcnt(13)
	v_mfma_f32_16x16x32_f16 a[32:35], v[10:13], v[14:17], a[32:35]
	v_mfma_f32_16x16x32_f16 a[40:43], v[10:13], v[18:21], a[40:43]
	s_waitcnt lgkmcnt(12)
	v_mfma_f32_16x16x32_f16 a[48:51], v[6:9], v[14:17], a[48:51]
	v_mfma_f32_16x16x32_f16 a[52:55], v[6:9], v[18:21], a[52:55]
	s_waitcnt lgkmcnt(11)
	v_mfma_f32_16x16x32_f16 a[56:59], v[2:5], v[14:17], a[56:59]
	v_mfma_f32_16x16x32_f16 a[68:71], v[2:5], v[18:21], a[68:71]
	s_waitcnt vmcnt(6) lgkmcnt(0)
	s_barrier
	v_add_u32_e32 v169, s16, v118
	s_nop 1
	v_readfirstlane_b32 s14, v169
	s_mov_b32 m0, s14
	s_nop 0
	global_load_lds_dwordx4 v[0:1], off nt
	v_add_u32_e32 v169, s16, v90
	s_nop 1
	v_readfirstlane_b32 s14, v169
	s_mov_b32 m0, s14
	s_nop 0
	global_load_lds_dwordx4 v[106:107], off nt
	v_add_u32_e32 v169, s16, v91
	s_nop 1
	v_readfirstlane_b32 s14, v169
	s_mov_b32 m0, s14
	s_nop 0
	global_load_lds_dwordx4 v[110:111], off nt
	v_add_u32_e32 v169, s16, v119
	s_nop 1
	v_readfirstlane_b32 s14, v169
	s_mov_b32 m0, s14
	s_nop 0
	global_load_lds_dwordx4 v[114:115], off nt
	s_add_u32 s52, s10, 0x1000000
	s_addc_u32 s53, s11, 0
	v_add_u32_e32 v169, 0xe000, v91
	v_lshlrev_b32_e32 v170, 2, v98
	s_nop 0
	v_readfirstlane_b32 s14, v169
	s_mov_b32 m0, s14
	s_nop 0
	global_load_lds_dwordx4 v170, s[52:53] nt
	v_add_u32_e32 v169, 0xe000, v119
	v_lshlrev_b32_e32 v170, 2, v100
	s_nop 0
	v_readfirstlane_b32 s14, v169
	s_mov_b32 m0, s14
	s_nop 0
	global_load_lds_dwordx4 v170, s[52:53] nt
	v_mfma_f32_16x16x32_f16 a[0:3], v[70:73], v[82:85], a[0:3]
	ds_read_b128 v[14:17], v160
	v_mfma_f32_16x16x32_f16 a[4:7], v[70:73], v[86:89], a[4:7]
	ds_read_b128 v[18:21], v162
	v_mfma_f32_16x16x32_f16 a[12:15], v[66:69], v[82:85], a[12:15]
	ds_read_b128 v[42:45], v164
	v_mfma_f32_16x16x32_f16 a[16:19], v[66:69], v[86:89], a[16:19]
	ds_read_b128 v[38:41], v164 offset:1024
	v_mfma_f32_16x16x32_f16 a[28:31], v[58:61], v[82:85], a[28:31]
	ds_read_b128 v[34:37], v164 offset:2048
	v_mfma_f32_16x16x32_f16 a[60:63], v[58:61], v[86:89], a[60:63]
	ds_read_b128 v[30:33], v164 offset:3072
	v_mfma_f32_16x16x32_f16 a[8:11], v[54:57], v[82:85], a[8:11]
	ds_read_b128 v[26:29], v164 offset:4096
	v_mfma_f32_16x16x32_f16 a[20:23], v[54:57], v[86:89], a[20:23]
	ds_read_b128 v[22:25], v164 offset:5120
	v_mfma_f32_16x16x32_f16 a[24:27], v[46:49], v[82:85], a[24:27]
	ds_read_b128 v[10:13], v164 offset:6144
	v_mfma_f32_16x16x32_f16 a[36:39], v[46:49], v[86:89], a[36:39]
	ds_read_b128 v[6:9], v164 offset:7168
	v_mfma_f32_16x16x32_f16 a[44:47], v[50:53], v[82:85], a[44:47]
	ds_read_b128 v[2:5], v164 offset:8192
	v_mfma_f32_16x16x32_f16 a[64:67], v[50:53], v[86:89], a[64:67]
	v_mfma_f32_16x16x32_f16 a[32:35], v[62:65], v[82:85], a[32:35]
	v_mfma_f32_16x16x32_f16 a[40:43], v[62:65], v[86:89], a[40:43]
	v_mfma_f32_16x16x32_f16 a[48:51], v[74:77], v[82:85], a[48:51]
	v_mfma_f32_16x16x32_f16 a[52:55], v[74:77], v[86:89], a[52:55]
	v_mfma_f32_16x16x32_f16 a[56:59], v[78:81], v[82:85], a[56:59]
	v_mfma_f32_16x16x32_f16 a[68:71], v[78:81], v[86:89], a[68:71]
	s_waitcnt lgkmcnt(8)
	v_mfma_f32_16x16x32_f16 a[0:3], v[42:45], v[14:17], a[0:3]
	ds_read_b128 v[82:85], v161
	v_mfma_f32_16x16x32_f16 a[4:7], v[42:45], v[18:21], a[4:7]
	ds_read_b128 v[86:89], v163
	s_waitcnt lgkmcnt(9)
	v_mfma_f32_16x16x32_f16 a[12:15], v[38:41], v[14:17], a[12:15]
	ds_read_b128 v[70:73], v164 offset:9216
	v_mfma_f32_16x16x32_f16 a[16:19], v[38:41], v[18:21], a[16:19]
	ds_read_b128 v[66:69], v164 offset:10240
	s_waitcnt lgkmcnt(10)
	v_mfma_f32_16x16x32_f16 a[28:31], v[34:37], v[14:17], a[28:31]
	ds_read_b128 v[58:61], v164 offset:11264
	v_mfma_f32_16x16x32_f16 a[60:63], v[34:37], v[18:21], a[60:63]
	ds_read_b128 v[54:57], v164 offset:12288
	s_waitcnt lgkmcnt(11)
	v_mfma_f32_16x16x32_f16 a[8:11], v[30:33], v[14:17], a[8:11]
	ds_read_b128 v[46:49], v164 offset:13312
	v_mfma_f32_16x16x32_f16 a[20:23], v[30:33], v[18:21], a[20:23]
	ds_read_b128 v[50:53], v164 offset:14336
	s_waitcnt lgkmcnt(12)
	v_mfma_f32_16x16x32_f16 a[24:27], v[26:29], v[14:17], a[24:27]
	ds_read_b128 v[62:65], v164 offset:15360
	v_mfma_f32_16x16x32_f16 a[36:39], v[26:29], v[18:21], a[36:39]
	ds_read_b128 v[74:77], v164 offset:16384
	s_waitcnt lgkmcnt(13)
	v_mfma_f32_16x16x32_f16 a[44:47], v[22:25], v[14:17], a[44:47]
	ds_read_b128 v[78:81], v164 offset:17408
	v_mfma_f32_16x16x32_f16 a[64:67], v[22:25], v[18:21], a[64:67]
	s_waitcnt lgkmcnt(13)
	v_mfma_f32_16x16x32_f16 a[32:35], v[10:13], v[14:17], a[32:35]
	v_mfma_f32_16x16x32_f16 a[40:43], v[10:13], v[18:21], a[40:43]
	s_waitcnt lgkmcnt(12)
	v_mfma_f32_16x16x32_f16 a[48:51], v[6:9], v[14:17], a[48:51]
	v_mfma_f32_16x16x32_f16 a[52:55], v[6:9], v[18:21], a[52:55]
	s_waitcnt lgkmcnt(11)
	v_mfma_f32_16x16x32_f16 a[56:59], v[2:5], v[14:17], a[56:59]
	v_mfma_f32_16x16x32_f16 a[68:71], v[2:5], v[18:21], a[68:71]
	s_waitcnt lgkmcnt(8)
	v_mfma_f32_16x16x32_f16 a[0:3], v[70:73], v[82:85], a[0:3]
	v_mfma_f32_16x16x32_f16 a[4:7], v[70:73], v[86:89], a[4:7]
	s_waitcnt lgkmcnt(9)
	v_mfma_f32_16x16x32_f16 a[12:15], v[66:69], v[82:85], a[12:15]
	v_mfma_f32_16x16x32_f16 a[16:19], v[66:69], v[86:89], a[16:19]
	s_waitcnt lgkmcnt(10)
	v_mfma_f32_16x16x32_f16 a[28:31], v[58:61], v[82:85], a[28:31]
	v_mfma_f32_16x16x32_f16 a[60:63], v[58:61], v[86:89], a[60:63]
	s_waitcnt lgkmcnt(11)
	v_mfma_f32_16x16x32_f16 a[8:11], v[54:57], v[82:85], a[8:11]
	v_mfma_f32_16x16x32_f16 a[20:23], v[54:57], v[86:89], a[20:23]
	s_waitcnt lgkmcnt(12)
	v_mfma_f32_16x16x32_f16 a[24:27], v[46:49], v[82:85], a[24:27]
	v_mfma_f32_16x16x32_f16 a[36:39], v[46:49], v[86:89], a[36:39]
	s_waitcnt lgkmcnt(13)
	v_mfma_f32_16x16x32_f16 a[44:47], v[50:53], v[82:85], a[44:47]
	v_mfma_f32_16x16x32_f16 a[64:67], v[50:53], v[86:89], a[64:67]
	s_waitcnt lgkmcnt(13)
	v_mfma_f32_16x16x32_f16 a[32:35], v[62:65], v[82:85], a[32:35]
	v_mfma_f32_16x16x32_f16 a[40:43], v[62:65], v[86:89], a[40:43]
	s_waitcnt lgkmcnt(12)
	v_mfma_f32_16x16x32_f16 a[48:51], v[74:77], v[82:85], a[48:51]
	v_mfma_f32_16x16x32_f16 a[52:55], v[74:77], v[86:89], a[52:55]
	s_waitcnt lgkmcnt(11)
	v_mfma_f32_16x16x32_f16 a[56:59], v[78:81], v[82:85], a[56:59]
	v_mfma_f32_16x16x32_f16 a[68:71], v[78:81], v[86:89], a[68:71]
	s_waitcnt lgkmcnt(0)
	s_setprio 0
.LBB3_32:
	s_barrier
	v_mbcnt_lo_u32_b32 v60, -1, 0
	v_mbcnt_hi_u32_b32 v60, -1, v60
	v_lshlrev_b32_e32 v60, 4, v60
	v_add_u32_e32 v61, v91, v60
	v_add_u32_e32 v62, v119, v60
	v_add_u32_e32 v63, v118, v60
	v_add_u32_e32 v64, v90, v60
	ds_write_b128 v61, v[128:131]
	ds_write_b128 v62, v[132:135]
	ds_write_b128 v63, v[172:175] offset:28672
	ds_write_b128 v64, v[176:179] offset:28672
	v_mov_b32_e32 v156, v61
	v_mov_b32_e32 v157, v62
	v_mov_b32_e32 v158, v63
	v_mov_b32_e32 v159, v64
	v_lshl_add_u32 v0, v120, 5, s22
	v_or_b32_e32 v1, s23, v121
	s_movk_i32 s0, 0x7f
	v_lshl_or_b32 v7, v93, 1, v0
	s_movk_i32 s1, 0x7e
	s_nop 15
	s_nop 15
	v_cmp_eq_u32_e64 s[4:5], s1, v7
	s_nop 7
	v_cmp_gt_u32_e32 vcc, s0, v1
	v_accvgpr_read_b32 v5, a14
	v_cmp_eq_u32_e64 s[0:1], 0, v1
	v_or_b32_e32 v4, v93, v7
	v_cmp_eq_u32_e64 s[2:3], 0, v4
	v_cndmask_b32_e64 v14, v5, 0, s[0:1]
	v_accvgpr_read_b32 v5, a13
	v_cndmask_b32_e64 v22, v5, 0, s[0:1]
	v_accvgpr_read_b32 v5, a12
	v_cndmask_b32_e64 v116, v5, 0, s[0:1]
	v_accvgpr_read_b32 v5, a49
	v_cndmask_b32_e32 v16, 0, v5, vcc
	v_accvgpr_read_b32 v5, a48
	v_cndmask_b32_e32 v28, 0, v5, vcc
	v_accvgpr_read_b32 v5, a30
	v_cndmask_b32_e64 v10, v5, 0, s[0:1]
	v_accvgpr_read_b32 v5, a29
	v_cndmask_b32_e64 v24, v5, 0, s[0:1]
	v_accvgpr_read_b32 v5, a28
	v_cndmask_b32_e64 v42, v5, 0, s[0:1]
	v_accvgpr_read_b32 v5, a57
	v_cndmask_b32_e32 v20, 0, v5, vcc
	v_accvgpr_read_b32 v5, a56
	v_cndmask_b32_e32 v38, 0, v5, vcc
	v_accvgpr_read_b32 v5, a6
	v_cndmask_b32_e64 v15, v5, 0, s[0:1]
	v_accvgpr_read_b32 v5, a5
	v_cndmask_b32_e64 v23, v5, 0, s[0:1]
	v_accvgpr_read_b32 v5, a4
	v_cndmask_b32_e64 v117, v5, 0, s[0:1]
	v_accvgpr_read_b32 v5, a41
	v_cndmask_b32_e32 v17, 0, v5, vcc
	v_accvgpr_read_b32 v5, a40
	v_cndmask_b32_e32 v29, 0, v5, vcc
	v_accvgpr_read_b32 v5, a17
	v_cndmask_b32_e64 v37, v5, 0, s[0:1]
	v_accvgpr_read_b32 v5, a16
	v_cndmask_b32_e64 v47, v5, 0, s[0:1]
	v_accvgpr_read_b32 v5, a52
	v_cndmask_b32_e32 v45, 0, v5, vcc
	v_accvgpr_read_b32 v5, a68
	v_cndmask_b32_e32 v12, 0, v5, vcc
	v_accvgpr_read_b32 v5, a0
	s_or_b64 s[8:9], s[2:3], s[0:1]
	v_cmp_eq_u32_e64 s[6:7], 15, v93
	v_accvgpr_read_b32 v11, a8
	v_cndmask_b32_e64 v112, v5, 0, s[8:9]
	v_accvgpr_read_b32 v4, a67
	v_mov_b32_e32 v5, 0x90
	s_and_b64 s[4:5], s[6:7], s[4:5]
	v_mov_b64_e32 v[40:41], v[16:17]
	v_cndmask_b32_e64 v16, v11, 0, s[2:3]
	v_cndmask_b32_e64 v11, 12, v5, s[6:7]
	v_cndmask_b32_e64 v61, v4, 0, s[4:5]
	v_accvgpr_read_b32 v4, a61
	s_or_b64 s[6:7], s[4:5], s[0:1]
	v_cndmask_b32_e64 v87, v4, 0, s[6:7]
	v_accvgpr_read_b32 v4, a60
	v_cndmask_b32_e64 v86, v4, 0, s[6:7]
	v_accvgpr_read_b32 v4, a65
	v_cndmask_b32_e64 v5, v4, 0, s[4:5]
	v_accvgpr_read_b32 v4, a64
	v_cndmask_b32_e64 v4, v4, 0, s[4:5]
	s_lshl_b32 s14, s18, 2
	v_mov_b64_e32 v[32:33], v[4:5]
	v_lshl_or_b32 v4, v122, 18, s14
	v_mov_b32_e32 v5, 0
	v_mov_b64_e32 v[62:63], v[14:15]
	v_lshl_add_u64 v[14:15], s[12:13], 0, v[4:5]
	v_lshlrev_b32_e32 v4, 7, v1
	v_lshl_add_u64 v[14:15], v[4:5], 2, v[14:15]
	v_lshlrev_b32_e32 v4, 2, v7
	v_mul_u32_u24_e32 v1, 24, v122
	v_lshl_add_u64 v[54:55], v[14:15], 0, v[4:5]
	v_mbcnt_lo_u32_b32 v138, -1, 0
	v_mbcnt_hi_u32_b32 v138, -1, v138
	v_and_b32_e32 v138, 1, v138
	v_mul_u32_u24_e32 v138, 0xfff8, v138
	v_add_u32_e32 v138, 0xffff0000, v138
	v_mov_b32_e32 v139, -1
	v_lshl_add_u64 v[134:135], v[54:55], 0, v[138:139]
	s_mov_b32 s28, 0x55555555
	s_mov_b32 s29, 0x55555555
	s_mov_b32 s30, 0xaaaaaaaa
	s_mov_b32 s31, 0xaaaaaaaa
	v_or_b32_e32 v1, v1, v121
	v_lshlrev_b32_e32 v4, 7, v120
	s_movk_i32 s12, 0x120
	v_mad_u32_u24 v1, v1, s12, v4
	s_add_u32 s12, s10, 0x800000
	v_accvgpr_read_b32 v7, a72
	v_mov_b64_e32 v[80:81], v[28:29]
	s_addc_u32 s13, s11, 0
	v_lshlrev_b64 v[28:29], 2, v[94:95]
	v_readfirstlane_b32 s14, v7
	v_add_u32_e32 v7, 0, v90
	v_lshl_add_u64 v[4:5], s[12:13], 0, v[28:29]
	s_mov_b32 m0, s14
	v_lshlrev_b64 v[30:31], 2, v[96:97]
	v_readfirstlane_b32 s14, v7
	v_mov_b32_e32 v14, v7
	v_add_u32_e32 v7, 0, v91
	s_waitcnt lgkmcnt(0)
	v_lshlrev_b64 v[56:57], 2, v[98:99]
	v_mov_b32_e32 v19, v7
	v_lshlrev_b64 v[58:59], 2, v[100:101]
	v_add_u32_e32 v7, 0, v119
	v_accvgpr_read_b32 v25, a72
	v_mov_b32_e32 v21, v7
	v_lshl_add_u32 v15, v93, 3, v1
	v_add_u32_e32 v1, v1, v11
	s_waitcnt vmcnt(16)
	v_accvgpr_write_b32 a12, v14
	v_mov_b64_e32 v[124:125], v[56:57]
	v_accvgpr_write_b32 a13, v19
	v_mov_b64_e32 v[126:127], v[58:59]
	v_accvgpr_write_b32 a16, v21
	s_waitcnt lgkmcnt(0)
	s_barrier
	v_add_u32_e32 v14, 0x16010, v15
	v_mov_b32_e32 v122, v15
	v_add_u32_e32 v15, 0x16000, v1
	ds_read_b64 v[64:65], v14
	ds_read_b64 v[66:67], v14 offset:288
	ds_read_b64 v[68:69], v14 offset:576
	ds_read_b64 v[76:77], v14 offset:1728
	ds_read_b64 v[78:79], v14 offset:2016
	ds_read_b64 v[4:5], v14 offset:2304
	ds_read_b64 v[84:85], v14 offset:3456
	ds_read_b64 v[74:75], v14 offset:3744
	ds_read_b64 v[88:89], v14 offset:4032
	ds_read_b64 v[100:101], v14 offset:5184
	ds_read_b64 v[106:107], v14 offset:5472
	ds_read_b64 v[120:121], v14 offset:5760
	ds_read_b32 v43, v15
	ds_read_b32 v19, v15 offset:288
	ds_read_b32 v39, v15 offset:576
	ds_read_b32 v25, v15 offset:1728
	ds_read_b32 v7, v15 offset:2016
	ds_read_b32 v21, v15 offset:2304
	ds_read_b32 v11, v15 offset:3456
	ds_read_b32 v35, v15 offset:3744
	ds_read_b32 v59, v15 offset:4032
	ds_read_b32 v57, v15 offset:5184
	ds_read_b32 v51, v15 offset:5472
	ds_read_b32 v49, v15 offset:5760
	s_waitcnt lgkmcnt(0)
	v_accvgpr_read_b32 v8, a26
	v_mov_b32_e32 v46, v43
	v_mov_b32_e32 v113, v65
	v_mov_b32_e32 v26, v19
	v_mov_b32_dpp v46, v65 row_shr:1 row_mask:0xf bank_mask:0xf
	v_pk_mul_f32 v[70:71], v[112:113], v[46:47]
	v_accvgpr_read_b32 v9, a22
	v_accvgpr_read_b32 v27, a36
	v_mov_b32_dpp v43, v64 row_shl:1 row_mask:0xf bank_mask:0xf
	v_mov_b32_dpp v26, v67 row_shr:1 row_mask:0xf bank_mask:0xf
	v_pk_fma_f32 v[70:71], v[64:65], v[116:117], v[70:71] op_sel_hi:[0,1,1]
	v_pk_mov_b32 v[64:65], v[64:65], v[86:87] op_sel:[1,0]
	v_mov_b32_e32 v17, v67
	v_mov_b64_e32 v[102:103], v[8:9]
	v_accvgpr_read_b32 v8, a25
	v_accvgpr_read_b32 v114, a24
	v_accvgpr_read_b32 v9, a21
	v_accvgpr_read_b32 v115, a20
	v_accvgpr_read_b32 v2, a32
	v_mov_b64_e32 v[82:83], v[30:31]
	v_pk_fma_f32 v[70:71], v[64:65], v[42:43], v[70:71]
	v_pk_mul_f32 v[64:65], v[16:17], v[26:27]
	v_mov_b64_e32 v[30:31], v[32:33]
	v_accvgpr_read_b32 v18, a44
	v_mov_b64_e32 v[104:105], v[8:9]
	v_cndmask_b32_e32 v9, 0, v2, vcc
	v_accvgpr_write_b32 a4, v14
	v_mov_b32_dpp v19, v66 row_shl:1 row_mask:0xf bank_mask:0xf
	v_pk_fma_f32 v[64:65], v[66:67], v[114:115], v[64:65] op_sel_hi:[0,1,1]
	v_pk_mov_b32 v[66:67], v[66:67], v[30:31] op_sel:[1,0]
	v_accvgpr_read_b32 v14, a69
	v_mov_b32_e32 v44, v39
	v_mov_b32_e32 v60, v1
	v_pk_fma_f32 v[66:67], v[66:67], v[18:19], v[64:65]
	v_cndmask_b32_e32 v14, 0, v14, vcc
	v_cndmask_b32_e64 v0, v9, 0, s[2:3]
	v_mov_b32_dpp v44, v69 row_shr:1 row_mask:0xf bank_mask:0xf
	v_pk_add_f32 v[70:71], v[70:71], 0 op_sel_hi:[1,0]
	v_mov_b32_e32 v1, v69
	v_accvgpr_write_b32 a0, v15
	v_cndmask_b32_e64 v15, v14, 0, s[4:5]
	v_cndmask_b32_e64 v14, v12, 0, s[4:5]
	v_pk_add_f32 v[66:67], v[70:71], v[66:67]
	v_pk_mul_f32 v[70:71], v[0:1], v[44:45]
	v_mov_b32_dpp v39, v68 row_shl:1 row_mask:0xf bank_mask:0xf
	v_pk_fma_f32 v[70:71], v[68:69], v[80:81], v[70:71] op_sel_hi:[0,1,1]
	v_pk_mov_b32 v[68:69], v[68:69], v[14:15] op_sel:[1,0]
	v_accvgpr_read_b32 v9, a1
	v_pk_fma_f32 v[68:69], v[68:69], v[38:39], v[70:71]
	v_mov_b32_e32 v36, v25
	v_cndmask_b32_e64 v64, v9, 0, s[8:9]
	v_pk_add_f32 v[66:67], v[66:67], v[68:69]
	v_mov_b32_dpp v36, v77 row_shr:1 row_mask:0xf bank_mask:0xf
	v_mov_b32_e32 v65, v77
	v_mov_b64_e32 v[108:109], v[22:23]
	v_accvgpr_read_b32 v9, a9
	v_mov_b32_e32 v128, v66
	v_mov_b32_e32 v129, v67
	v_mov_b32_e32 v12, v7
	v_pk_mul_f32 v[66:67], v[64:65], v[36:37]
	v_accvgpr_read_b32 v13, a37
	v_mov_b64_e32 v[72:73], v[28:29]
	v_cndmask_b32_e64 v28, v9, 0, s[2:3]
	v_mov_b32_dpp v25, v76 row_shl:1 row_mask:0xf bank_mask:0xf
	v_mov_b32_dpp v12, v79 row_shr:1 row_mask:0xf bank_mask:0xf
	v_pk_fma_f32 v[66:67], v[76:77], v[108:109], v[66:67] op_sel_hi:[0,1,1]
	v_mov_b32_e32 v76, v77
	v_mov_b32_e32 v77, v87
	v_mov_b32_e32 v29, v79
	v_pk_fma_f32 v[66:67], v[76:77], v[24:25], v[66:67]
	v_pk_mul_f32 v[76:77], v[28:29], v[12:13]
	v_accvgpr_read_b32 v6, a45
	v_accvgpr_read_b32 v2, a33
	v_mov_b32_dpp v7, v78 row_shl:1 row_mask:0xf bank_mask:0xf
	v_pk_fma_f32 v[76:77], v[78:79], v[104:105], v[76:77] op_sel_hi:[0,1,1]
	v_mov_b32_e32 v78, v79
	v_mov_b32_e32 v79, v31
	v_cndmask_b32_e32 v2, 0, v2, vcc
	v_accvgpr_read_b32 v50, a53
	v_pk_fma_f32 v[76:77], v[78:79], v[6:7], v[76:77]
	v_mov_b32_e32 v78, v21
	v_accvgpr_write_b32 a44, v80
	v_cndmask_b32_e32 v79, 0, v50, vcc
	v_cndmask_b32_e64 v52, v2, 0, s[2:3]
	v_mov_b32_dpp v78, v5 row_shr:1 row_mask:0xf bank_mask:0xf
	v_pk_add_f32 v[66:67], v[66:67], 0 op_sel_hi:[1,0]
	v_mov_b32_e32 v53, v5
	v_accvgpr_write_b32 a45, v81
	v_accvgpr_write_b32 a21, v15
	v_pk_add_f32 v[80:81], v[66:67], v[76:77]
	v_pk_mul_f32 v[66:67], v[52:53], v[78:79]
	v_accvgpr_write_b32 a24, v40
	v_accvgpr_read_b32 v2, a2
	v_mov_b32_dpp v21, v4 row_shl:1 row_mask:0xf bank_mask:0xf
	v_pk_fma_f32 v[66:67], v[4:5], v[40:41], v[66:67] op_sel_hi:[0,1,1]
	v_accvgpr_write_b32 a25, v41
	v_mov_b32_e32 v4, v5
	v_accvgpr_read_b32 v5, a21
	v_cndmask_b32_e64 v40, v2, 0, s[8:9]
	v_accvgpr_read_b32 v2, a62
	v_accvgpr_read_b32 v8, a18
	v_accvgpr_read_b32 v48, a63
	v_accvgpr_write_b32 a20, v14
	v_accvgpr_write_b32 a41, v23
	v_pk_fma_f32 v[4:5], v[4:5], v[20:21], v[66:67]
	s_mov_b64 s[12:13], 0x10000
	v_cndmask_b32_e64 v14, v2, 0, s[6:7]
	v_mov_b32_e32 v76, v11
	v_accvgpr_read_b32 v2, a10
	v_accvgpr_write_b32 a40, v22
	v_cndmask_b32_e64 v15, v48, 0, s[6:7]
	v_cndmask_b32_e64 v77, v8, 0, s[0:1]
	v_pk_add_f32 v[4:5], v[80:81], v[4:5]
	v_lshl_add_u64 v[136:137], v[134:135], 0, s[12:13]
	v_mov_b32_dpp v76, v85 row_shr:1 row_mask:0xf bank_mask:0xf
	v_mov_b32_e32 v41, v85
	v_cndmask_b32_e64 v22, v2, 0, s[2:3]
	v_mov_b32_e32 v2, v35
	v_accvgpr_read_b32 v1, a50
	v_accvgpr_read_b32 v3, a38
	s_mov_b64 s[32:33], vcc
	s_nop 1
	s_mov_b64 vcc, s[28:29]
	s_nop 0
	v_cndmask_b32_dpp v130, v4, v128, vcc quad_perm:[1,0,3,2] row_mask:0xf bank_mask:0xf
	v_cndmask_b32_dpp v131, v5, v129, vcc quad_perm:[1,0,3,2] row_mask:0xf bank_mask:0xf
	s_mov_b64 vcc, s[30:31]
	s_nop 0
	v_cndmask_b32_dpp v132, v128, v4, vcc quad_perm:[1,0,3,2] row_mask:0xf bank_mask:0xf
	v_cndmask_b32_dpp v133, v129, v5, vcc quad_perm:[1,0,3,2] row_mask:0xf bank_mask:0xf
	global_store_dwordx4 v[136:137], v[130:133], off sc0 sc1 nt
	s_nop 1
	s_mov_b64 vcc, s[32:33]
	v_mov_b64_e32 v[8:9], v[14:15]
	v_pk_mul_f32 v[4:5], v[40:41], v[76:77]
	v_mov_b64_e32 v[66:67], v[62:63]
	v_mov_b32_dpp v2, v75 row_shr:1 row_mask:0xf bank_mask:0xf
	v_mov_b32_e32 v23, v75
	v_cndmask_b32_e32 v62, 0, v1, vcc
	v_accvgpr_read_b32 v1, a42
	v_mov_b32_dpp v11, v84 row_shl:1 row_mask:0xf bank_mask:0xf
	v_pk_fma_f32 v[4:5], v[84:85], v[66:67], v[4:5] op_sel_hi:[0,1,1]
	v_pk_mov_b32 v[80:81], v[84:85], v[8:9] op_sel:[1,0]
	v_pk_mul_f32 v[84:85], v[22:23], v[2:3]
	v_accvgpr_read_b32 v2, a58
	v_cndmask_b32_e32 v63, 0, v1, vcc
	v_accvgpr_read_b32 v1, a70
	v_pk_fma_f32 v[80:81], v[80:81], v[10:11], v[4:5]
	v_accvgpr_read_b32 v4, a66
	v_cndmask_b32_e32 v58, 0, v2, vcc
	v_cndmask_b32_e32 v1, 0, v1, vcc
	v_accvgpr_read_b32 v2, a71
	v_cndmask_b32_e64 v8, v4, 0, s[4:5]
	v_cndmask_b32_e32 v2, 0, v2, vcc
	v_cndmask_b32_e64 v4, v1, 0, s[4:5]
	v_accvgpr_read_b32 v1, a34
	v_mov_b32_e32 v9, v61
	v_cndmask_b32_e64 v5, v2, 0, s[4:5]
	v_cndmask_b32_e32 v1, 0, v1, vcc
	v_accvgpr_read_b32 v2, a54
	v_mov_b32_e32 v92, v59
	v_accvgpr_read_b32 v34, a46
	v_mov_b32_dpp v35, v74 row_shl:1 row_mask:0xf bank_mask:0xf
	v_pk_fma_f32 v[84:85], v[74:75], v[102:103], v[84:85] op_sel_hi:[0,1,1]
	v_pk_mov_b32 v[74:75], v[74:75], v[8:9] op_sel:[1,0]
	v_cndmask_b32_e32 v93, 0, v2, vcc
	v_mov_b32_dpp v92, v89 row_shr:1 row_mask:0xf bank_mask:0xf
	v_cndmask_b32_e64 v96, v1, 0, s[2:3]
	v_mov_b32_e32 v97, v89
	v_accvgpr_read_b32 v1, a31
	v_pk_fma_f32 v[74:75], v[74:75], v[34:35], v[84:85]
	v_pk_mul_f32 v[84:85], v[96:97], v[92:93]
	v_accvgpr_write_b32 a8, v62
	v_cndmask_b32_e64 v56, v1, 0, s[0:1]
	v_accvgpr_read_b32 v1, a15
	v_pk_fma_f32 v[84:85], v[88:89], v[62:63], v[84:85] op_sel_hi:[0,1,1]
	v_accvgpr_write_b32 a9, v63
	v_cndmask_b32_e64 v62, v1, 0, s[0:1]
	v_accvgpr_read_b32 v1, a7
	v_cndmask_b32_e64 v63, v1, 0, s[0:1]
	v_accvgpr_read_b32 v1, a19
	v_pk_add_f32 v[80:81], v[80:81], 0 op_sel_hi:[1,0]
	v_mov_b32_dpp v59, v88 row_shl:1 row_mask:0xf bank_mask:0xf
	v_pk_mov_b32 v[88:89], v[88:89], v[4:5] op_sel:[1,0]
	v_cndmask_b32_e64 v95, v1, 0, s[0:1]
	v_accvgpr_read_b32 v1, a3
	v_accvgpr_write_b32 a36, v104
	v_pk_add_f32 v[80:81], v[80:81], v[74:75]
	v_pk_fma_f32 v[84:85], v[88:89], v[58:59], v[84:85]
	v_mov_b32_e32 v94, v57
	v_cndmask_b32_e64 v98, v1, 0, s[8:9]
	v_accvgpr_read_b32 v1, a11
	v_accvgpr_write_b32 a37, v105
	v_accvgpr_write_b32 a32, v102
	v_pk_add_f32 v[80:81], v[80:81], v[84:85]
	s_mov_b64 s[4:5], 0x20000
	v_mov_b32_dpp v94, v101 row_shr:1 row_mask:0xf bank_mask:0xf
	v_mov_b32_e32 v99, v101
	v_cndmask_b32_e64 v104, v1, 0, s[2:3]
	v_accvgpr_read_b32 v1, a59
	v_accvgpr_write_b32 a29, v15
	v_accvgpr_write_b32 a33, v103
	v_accvgpr_write_b32 a49, v5
	v_lshl_add_u64 v[84:85], v[54:55], 0, s[4:5]
	v_mov_b32_e32 v128, v80
	v_mov_b32_e32 v129, v81
	v_pk_mul_f32 v[80:81], v[98:99], v[94:95]
	v_mov_b32_e32 v102, v51
	v_cndmask_b32_e32 v48, 0, v1, vcc
	v_accvgpr_read_b32 v1, a51
	v_accvgpr_write_b32 a48, v4
	v_mov_b32_dpp v57, v100 row_shl:1 row_mask:0xf bank_mask:0xf
	v_pk_fma_f32 v[80:81], v[100:101], v[62:63], v[80:81] op_sel_hi:[0,1,1]
	v_mov_b32_e32 v84, v101
	v_accvgpr_read_b32 v85, a29
	v_accvgpr_read_b32 v103, a39
	v_mov_b32_dpp v102, v107 row_shr:1 row_mask:0xf bank_mask:0xf
	v_mov_b32_e32 v105, v107
	v_cndmask_b32_e32 v4, 0, v1, vcc
	v_accvgpr_read_b32 v1, a43
	v_pk_fma_f32 v[80:81], v[84:85], v[56:57], v[80:81]
	v_accvgpr_read_b32 v30, a27
	v_accvgpr_read_b32 v31, a23
	v_pk_mul_f32 v[84:85], v[104:105], v[102:103]
	v_cndmask_b32_e32 v5, 0, v1, vcc
	v_accvgpr_read_b32 v1, a35
	v_accvgpr_read_b32 v50, a47
	v_mov_b32_dpp v51, v106 row_shl:1 row_mask:0xf bank_mask:0xf
	v_pk_fma_f32 v[84:85], v[106:107], v[30:31], v[84:85] op_sel_hi:[0,1,1]
	v_mov_b32_e32 v106, v107
	v_mov_b32_e32 v107, v9
	v_cndmask_b32_e32 v1, 0, v1, vcc
	v_accvgpr_read_b32 v2, a55
	v_mov_b32_e32 v108, v49
	v_pk_fma_f32 v[84:85], v[106:107], v[50:51], v[84:85]
	v_pk_add_f32 v[80:81], v[80:81], 0 op_sel_hi:[1,0]
	v_cndmask_b32_e32 v109, 0, v2, vcc
	v_mov_b32_dpp v108, v121 row_shr:1 row_mask:0xf bank_mask:0xf
	v_cndmask_b32_e64 v110, v1, 0, s[2:3]
	v_mov_b32_e32 v111, v121
	v_pk_add_f32 v[80:81], v[80:81], v[84:85]
	v_pk_mul_f32 v[84:85], v[110:111], v[108:109]
	v_mov_b32_dpp v49, v120 row_shl:1 row_mask:0xf bank_mask:0xf
	v_pk_fma_f32 v[84:85], v[120:121], v[4:5], v[84:85] op_sel_hi:[0,1,1]
	v_mov_b32_e32 v120, v121
	v_accvgpr_read_b32 v121, a49
	v_pk_fma_f32 v[84:85], v[120:121], v[48:49], v[84:85]
	s_mov_b64 s[0:1], 0x30000
	v_pk_add_f32 v[80:81], v[80:81], v[84:85]
	v_lshl_add_u64 v[136:137], v[134:135], 0, s[0:1]
	v_add_u32_e32 v1, s17, v118
	s_add_u32 s0, s10, 0x1400000
	s_mov_b64 s[32:33], vcc
	s_nop 1
	s_mov_b64 vcc, s[28:29]
	s_nop 0
	v_cndmask_b32_dpp v130, v80, v128, vcc quad_perm:[1,0,3,2] row_mask:0xf bank_mask:0xf
	v_cndmask_b32_dpp v131, v81, v129, vcc quad_perm:[1,0,3,2] row_mask:0xf bank_mask:0xf
	s_mov_b64 vcc, s[30:31]
	s_nop 0
	v_cndmask_b32_dpp v132, v128, v80, vcc quad_perm:[1,0,3,2] row_mask:0xf bank_mask:0xf
	v_cndmask_b32_dpp v133, v129, v81, vcc quad_perm:[1,0,3,2] row_mask:0xf bank_mask:0xf
	global_store_dwordx4 v[136:137], v[130:133], off sc0 sc1 nt
	s_nop 1
	s_mov_b64 vcc, s[32:33]
	v_readfirstlane_b32 s2, v1
	s_addc_u32 s1, s11, 0
	v_add_u32_e32 v1, s17, v90
	s_waitcnt vmcnt(4)
	ds_write_b128 v156, v[140:143] offset:28672
	ds_write_b128 v157, v[144:147] offset:28672
	ds_write_b128 v158, v[148:151] offset:57344
	ds_write_b128 v159, v[152:155] offset:57344
	v_lshl_add_u64 v[80:81], s[0:1], 0, v[72:73]
	s_mov_b32 m0, s2
	v_readfirstlane_b32 s2, v1
	v_mov_b64_e32 v[74:75], v[82:83]
	v_add_u32_e32 v1, s17, v91
	s_waitcnt lgkmcnt(0)
	s_barrier
	global_load_lds_dwordx4 v[80:81], off nt
	v_lshl_add_u64 v[80:81], s[0:1], 0, v[74:75]
	s_mov_b32 m0, s2
	v_readfirstlane_b32 s2, v1
	v_add_u32_e32 v1, s17, v119
	global_load_lds_dwordx4 v[80:81], off nt
	v_lshl_add_u64 v[80:81], s[0:1], 0, v[124:125]
	s_mov_b32 m0, s2
	v_readfirstlane_b32 s2, v1
	global_load_lds_dwordx4 v[80:81], off nt
	v_lshl_add_u64 v[80:81], s[0:1], 0, v[126:127]
	s_mov_b32 m0, s2
	v_accvgpr_write_b32 a53, v33
	v_accvgpr_write_b32 a2, v62
	v_accvgpr_write_b32 a7, v5
	v_accvgpr_write_b32 a22, v124
	v_accvgpr_write_b32 a30, v126
	global_load_lds_dwordx4 v[80:81], off nt
	v_accvgpr_write_b32 a52, v32
	v_accvgpr_write_b32 a3, v63
	v_accvgpr_write_b32 a6, v4
	v_mov_b64_e32 v[32:33], v[72:73]
	v_accvgpr_write_b32 a23, v125
	v_accvgpr_write_b32 a31, v127
	v_add_u32_e32 v2, 0x1d010, v122
	v_accvgpr_write_b32 a10, v122
	v_add_u32_e32 v5, 0x1d000, v60
	v_mov_b32_e32 v4, v60
	ds_read_b64 v[62:63], v2
	ds_read_b64 v[60:61], v2 offset:288
	ds_read_b64 v[72:73], v2 offset:576
	ds_read_b64 v[70:71], v2 offset:1728
	ds_read_b64 v[68:69], v2 offset:2016
	ds_read_b64 v[82:83], v2 offset:2304
	ds_read_b64 v[80:81], v2 offset:3456
	ds_read_b64 v[84:85], v2 offset:3744
	ds_read_b64 v[126:127], v2 offset:4032
	ds_read_b64 v[124:125], v2 offset:5184
	ds_read_b64 v[122:123], v2 offset:5472
	ds_read_b64 v[120:121], v2 offset:5760
	ds_read_b32 v43, v5
	ds_read_b32 v19, v5 offset:288
	ds_read_b32 v39, v5 offset:576
	ds_read_b32 v25, v5 offset:1728
	ds_read_b32 v7, v5 offset:2016
	ds_read_b32 v21, v5 offset:2304
	ds_read_b32 v11, v5 offset:3456
	ds_read_b32 v35, v5 offset:3744
	ds_read_b32 v59, v5 offset:4032
	ds_read_b32 v57, v5 offset:5184
	ds_read_b32 v51, v5 offset:5472
	ds_read_b32 v49, v5 offset:5760
	s_waitcnt lgkmcnt(0)
	v_mov_b64_e32 v[100:101], v[86:87]
	v_mov_b32_e32 v46, v43
	v_mov_b32_e32 v113, v63
	v_mov_b32_e32 v26, v19
	v_mov_b32_dpp v46, v63 row_shr:1 row_mask:0xf bank_mask:0xf
	v_pk_mul_f32 v[88:89], v[112:113], v[46:47]
	v_mov_b32_dpp v43, v62 row_shl:1 row_mask:0xf bank_mask:0xf
	v_pk_fma_f32 v[88:89], v[62:63], v[116:117], v[88:89] op_sel_hi:[0,1,1]
	v_pk_mov_b32 v[62:63], v[62:63], v[100:101] op_sel:[1,0]
	v_mov_b32_dpp v26, v61 row_shr:1 row_mask:0xf bank_mask:0xf
	v_mov_b32_e32 v17, v61
	v_pk_fma_f32 v[62:63], v[62:63], v[42:43], v[88:89]
	v_pk_mul_f32 v[88:89], v[16:17], v[26:27]
	v_accvgpr_write_b32 a34, v16
	v_accvgpr_read_b32 v16, a52
	v_accvgpr_read_b32 v17, a53
	v_mov_b32_dpp v19, v60 row_shl:1 row_mask:0xf bank_mask:0xf
	v_pk_fma_f32 v[88:89], v[60:61], v[114:115], v[88:89] op_sel_hi:[0,1,1]
	v_pk_mov_b32 v[60:61], v[60:61], v[16:17] op_sel:[1,0]
	v_mov_b32_e32 v44, v39
	v_accvgpr_write_b32 a28, v14
	v_pk_fma_f32 v[60:61], v[60:61], v[18:19], v[88:89]
	v_pk_add_f32 v[62:63], v[62:63], 0 op_sel_hi:[1,0]
	v_mov_b32_dpp v44, v73 row_shr:1 row_mask:0xf bank_mask:0xf
	v_mov_b32_e32 v1, v73
	v_accvgpr_read_b32 v14, a44
	v_accvgpr_read_b32 v89, a21
	v_pk_add_f32 v[60:61], v[62:63], v[60:61]
	v_pk_mul_f32 v[62:63], v[0:1], v[44:45]
	v_accvgpr_read_b32 v15, a45
	v_accvgpr_read_b32 v88, a20
	v_mov_b32_dpp v39, v72 row_shl:1 row_mask:0xf bank_mask:0xf
	v_pk_fma_f32 v[62:63], v[72:73], v[14:15], v[62:63] op_sel_hi:[0,1,1]
	v_pk_mov_b32 v[72:73], v[72:73], v[88:89] op_sel:[1,0]
	v_mov_b32_e32 v36, v25
	v_pk_fma_f32 v[62:63], v[72:73], v[38:39], v[62:63]
	s_mov_b64 s[0:1], 0x400000
	v_pk_add_f32 v[60:61], v[60:61], v[62:63]
	v_mov_b32_dpp v36, v71 row_shr:1 row_mask:0xf bank_mask:0xf
	v_mov_b32_e32 v65, v71
	v_accvgpr_read_b32 v87, a41
	v_lshl_add_u64 v[62:63], v[54:55], 0, s[0:1]
	v_mov_b32_e32 v128, v60
	v_mov_b32_e32 v129, v61
	v_pk_mul_f32 v[60:61], v[64:65], v[36:37]
	v_accvgpr_read_b32 v86, a40
	v_mov_b32_e32 v12, v7
	v_mov_b32_dpp v25, v70 row_shl:1 row_mask:0xf bank_mask:0xf
	v_pk_fma_f32 v[60:61], v[70:71], v[86:87], v[60:61] op_sel_hi:[0,1,1]
	v_mov_b32_e32 v62, v71
	v_mov_b32_e32 v63, v101
	v_mov_b32_dpp v12, v69 row_shr:1 row_mask:0xf bank_mask:0xf
	v_mov_b32_e32 v29, v69
	v_accvgpr_read_b32 v107, a37
	v_pk_fma_f32 v[60:61], v[62:63], v[24:25], v[60:61]
	v_pk_mul_f32 v[62:63], v[28:29], v[12:13]
	v_accvgpr_read_b32 v106, a36
	v_mov_b32_dpp v7, v68 row_shl:1 row_mask:0xf bank_mask:0xf
	v_pk_fma_f32 v[62:63], v[68:69], v[106:107], v[62:63] op_sel_hi:[0,1,1]
	v_mov_b32_e32 v68, v69
	v_mov_b32_e32 v69, v17
	v_mov_b32_e32 v78, v21
	v_pk_fma_f32 v[62:63], v[68:69], v[6:7], v[62:63]
	v_pk_add_f32 v[60:61], v[60:61], 0 op_sel_hi:[1,0]
	v_mov_b32_dpp v78, v83 row_shr:1 row_mask:0xf bank_mask:0xf
	v_mov_b32_e32 v53, v83
	v_accvgpr_read_b32 v14, a24
	v_pk_add_f32 v[60:61], v[60:61], v[62:63]
	v_pk_mul_f32 v[62:63], v[52:53], v[78:79]
	v_accvgpr_read_b32 v15, a25
	v_mov_b32_dpp v21, v82 row_shl:1 row_mask:0xf bank_mask:0xf
	v_pk_fma_f32 v[62:63], v[82:83], v[14:15], v[62:63] op_sel_hi:[0,1,1]
	v_mov_b32_e32 v68, v83
	v_mov_b32_e32 v69, v89
	v_pk_fma_f32 v[62:63], v[68:69], v[20:21], v[62:63]
	v_mov_b32_e32 v76, v11
	v_pk_add_f32 v[60:61], v[60:61], v[62:63]
	s_mov_b64 s[0:1], 0x410000
	v_mov_b32_dpp v76, v81 row_shr:1 row_mask:0xf bank_mask:0xf
	v_mov_b32_e32 v41, v81
	v_lshl_add_u64 v[136:137], v[134:135], 0, s[0:1]
	s_nop 1
	s_mov_b64 vcc, s[28:29]
	s_nop 0
	v_cndmask_b32_dpp v130, v60, v128, vcc quad_perm:[1,0,3,2] row_mask:0xf bank_mask:0xf
	v_cndmask_b32_dpp v131, v61, v129, vcc quad_perm:[1,0,3,2] row_mask:0xf bank_mask:0xf
	s_mov_b64 vcc, s[30:31]
	s_nop 0
	v_cndmask_b32_dpp v132, v128, v60, vcc quad_perm:[1,0,3,2] row_mask:0xf bank_mask:0xf
	v_cndmask_b32_dpp v133, v129, v61, vcc quad_perm:[1,0,3,2] row_mask:0xf bank_mask:0xf
	global_store_dwordx4 v[136:137], v[130:133], off sc0 sc1 nt
	s_nop 1
	v_pk_mul_f32 v[60:61], v[40:41], v[76:77]
	v_accvgpr_write_b32 a36, v66
	v_pk_fma_f32 v[60:61], v[80:81], v[66:67], v[60:61] op_sel_hi:[0,1,1]
	v_accvgpr_write_b32 a37, v67
	v_accvgpr_read_b32 v67, a29
	v_accvgpr_write_b32 a5, v2
	v_accvgpr_write_b32 a38, v100
	v_accvgpr_read_b32 v66, a28
	v_mov_b32_e32 v2, v35
	v_accvgpr_write_b32 a39, v101
	v_mov_b32_dpp v11, v80 row_shl:1 row_mask:0xf bank_mask:0xf
	v_pk_mov_b32 v[62:63], v[80:81], v[66:67] op_sel:[1,0]
	v_mov_b32_dpp v2, v85 row_shr:1 row_mask:0xf bank_mask:0xf
	v_mov_b32_e32 v23, v85
	v_accvgpr_read_b32 v101, a33
	v_pk_fma_f32 v[60:61], v[62:63], v[10:11], v[60:61]
	v_pk_mul_f32 v[62:63], v[22:23], v[2:3]
	v_accvgpr_read_b32 v100, a32
	v_mov_b32_dpp v35, v84 row_shl:1 row_mask:0xf bank_mask:0xf
	v_pk_fma_f32 v[62:63], v[84:85], v[100:101], v[62:63] op_sel_hi:[0,1,1]
	v_pk_mov_b32 v[68:69], v[84:85], v[8:9] op_sel:[1,0]
	v_mov_b32_e32 v92, v59
	v_pk_fma_f32 v[62:63], v[68:69], v[34:35], v[62:63]
	v_pk_add_f32 v[60:61], v[60:61], 0 op_sel_hi:[1,0]
	v_mov_b32_dpp v92, v127 row_shr:1 row_mask:0xf bank_mask:0xf
	v_mov_b32_e32 v97, v127
	v_accvgpr_read_b32 v17, a9
	v_accvgpr_read_b32 v71, a49
	v_pk_add_f32 v[60:61], v[60:61], v[62:63]
	v_pk_mul_f32 v[62:63], v[96:97], v[92:93]
	v_accvgpr_read_b32 v16, a8
	v_accvgpr_read_b32 v70, a48
	v_mov_b32_dpp v59, v126 row_shl:1 row_mask:0xf bank_mask:0xf
	v_pk_fma_f32 v[62:63], v[126:127], v[16:17], v[62:63] op_sel_hi:[0,1,1]
	v_pk_mov_b32 v[68:69], v[126:127], v[70:71] op_sel:[1,0]
	v_mov_b32_e32 v94, v57
	v_pk_fma_f32 v[62:63], v[68:69], v[58:59], v[62:63]
	v_accvgpr_write_b32 a20, v28
	v_pk_add_f32 v[60:61], v[60:61], v[62:63]
	s_mov_b64 s[0:1], 0x420000
	v_mov_b32_dpp v94, v125 row_shr:1 row_mask:0xf bank_mask:0xf
	v_mov_b32_e32 v99, v125
	v_accvgpr_read_b32 v29, a3
	v_lshl_add_u64 v[62:63], v[54:55], 0, s[0:1]
	v_mov_b32_e32 v128, v60
	v_mov_b32_e32 v129, v61
	v_pk_mul_f32 v[60:61], v[98:99], v[94:95]
	v_accvgpr_read_b32 v28, a2
	v_mov_b32_e32 v102, v51
	v_mov_b32_dpp v57, v124 row_shl:1 row_mask:0xf bank_mask:0xf
	v_pk_fma_f32 v[60:61], v[124:125], v[28:29], v[60:61] op_sel_hi:[0,1,1]
	v_mov_b32_e32 v62, v125
	v_mov_b32_e32 v63, v67
	v_mov_b32_dpp v102, v123 row_shr:1 row_mask:0xf bank_mask:0xf
	v_mov_b32_e32 v105, v123
	v_pk_fma_f32 v[60:61], v[62:63], v[56:57], v[60:61]
	v_pk_mul_f32 v[62:63], v[104:105], v[102:103]
	v_mov_b32_dpp v51, v122 row_shl:1 row_mask:0xf bank_mask:0xf
	v_pk_fma_f32 v[62:63], v[122:123], v[30:31], v[62:63] op_sel_hi:[0,1,1]
	v_accvgpr_write_b32 a28, v30
	v_mov_b32_e32 v68, v123
	v_mov_b32_e32 v69, v9
	v_mov_b32_e32 v108, v49
	v_accvgpr_write_b32 a29, v31
	v_pk_fma_f32 v[62:63], v[68:69], v[50:51], v[62:63]
	v_pk_add_f32 v[60:61], v[60:61], 0 op_sel_hi:[1,0]
	v_mov_b32_dpp v108, v121 row_shr:1 row_mask:0xf bank_mask:0xf
	v_mov_b32_e32 v111, v121
	v_accvgpr_read_b32 v31, a7
	v_pk_add_f32 v[60:61], v[60:61], v[62:63]
	v_pk_mul_f32 v[62:63], v[110:111], v[108:109]
	v_accvgpr_read_b32 v30, a6
	v_mov_b32_dpp v49, v120 row_shl:1 row_mask:0xf bank_mask:0xf
	v_pk_fma_f32 v[62:63], v[120:121], v[30:31], v[62:63] op_sel_hi:[0,1,1]
	v_mov_b32_e32 v68, v121
	v_mov_b32_e32 v69, v71
	v_pk_fma_f32 v[62:63], v[68:69], v[48:49], v[62:63]
	s_mov_b64 s[0:1], 0x430000
	v_pk_add_f32 v[60:61], v[60:61], v[62:63]
	v_lshl_add_u64 v[136:137], v[134:135], 0, s[0:1]
	v_add_u32_e32 v1, s16, v118
	s_add_u32 s0, s10, 0x1800000
	v_accvgpr_write_b32 a26, v114
	s_nop 1
	s_mov_b64 vcc, s[28:29]
	s_nop 0
	v_cndmask_b32_dpp v130, v60, v128, vcc quad_perm:[1,0,3,2] row_mask:0xf bank_mask:0xf
	v_cndmask_b32_dpp v131, v61, v129, vcc quad_perm:[1,0,3,2] row_mask:0xf bank_mask:0xf
	s_mov_b64 vcc, s[30:31]
	s_nop 0
	v_cndmask_b32_dpp v132, v128, v60, vcc quad_perm:[1,0,3,2] row_mask:0xf bank_mask:0xf
	v_cndmask_b32_dpp v133, v129, v61, vcc quad_perm:[1,0,3,2] row_mask:0xf bank_mask:0xf
	global_store_dwordx4 v[136:137], v[130:133], off sc0 sc1 nt
	s_nop 1
	v_readfirstlane_b32 s2, v1
	s_addc_u32 s1, s11, 0
	v_add_u32_e32 v1, s16, v90
	v_accvgpr_write_b32 a18, v116
	v_accvgpr_write_b32 a27, v115
	s_waitcnt vmcnt(16)
	v_lshl_add_u64 v[60:61], s[0:1], 0, v[32:33]
	s_mov_b32 m0, s2
	v_readfirstlane_b32 s2, v1
	v_add_u32_e32 v1, s16, v91
	v_accvgpr_read_b32 v115, a23
	v_accvgpr_write_b32 a19, v117
	s_waitcnt lgkmcnt(0)
	s_barrier
	global_load_lds_dwordx4 v[60:61], off nt
	v_lshl_add_u64 v[60:61], s[0:1], 0, v[74:75]
	s_mov_b32 m0, s2
	v_readfirstlane_b32 s2, v1
	v_accvgpr_read_b32 v114, a22
	v_add_u32_e32 v1, s16, v119
	v_accvgpr_read_b32 v117, a31
	global_load_lds_dwordx4 v[60:61], off nt
	v_lshl_add_u64 v[60:61], s[0:1], 0, v[114:115]
	s_mov_b32 m0, s2
	v_readfirstlane_b32 s2, v1
	v_accvgpr_read_b32 v116, a30
	global_load_lds_dwordx4 v[60:61], off nt
	v_lshl_add_u64 v[60:61], s[0:1], 0, v[116:117]
	s_mov_b32 m0, s2
	v_accvgpr_write_b32 a1, v5
	global_load_lds_dwordx4 v[60:61], off nt
	v_accvgpr_read_b32 v5, a10
	v_add_u32_e32 v2, 16, v5
	ds_read_b64 v[60:61], v2
	ds_read_b64 v[62:63], v2 offset:288
	ds_read_b64 v[68:69], v2 offset:576
	ds_read_b64 v[70:71], v2 offset:1728
	ds_read_b64 v[72:73], v2 offset:2016
	ds_read_b64 v[82:83], v2 offset:2304
	ds_read_b64 v[80:81], v2 offset:3456
	ds_read_b64 v[84:85], v2 offset:3744
	ds_read_b64 v[124:125], v2 offset:4032
	ds_read_b64 v[122:123], v2 offset:5184
	ds_read_b64 v[120:121], v2 offset:5472
	ds_read_b64 v[90:91], v2 offset:5760
	ds_read_b32 v43, v4
	ds_read_b32 v19, v4 offset:288
	ds_read_b32 v39, v4 offset:576
	ds_read_b32 v25, v4 offset:1728
	ds_read_b32 v7, v4 offset:2016
	ds_read_b32 v21, v4 offset:2304
	ds_read_b32 v11, v4 offset:3456
	ds_read_b32 v35, v4 offset:3744
	ds_read_b32 v59, v4 offset:4032
	ds_read_b32 v57, v4 offset:5184
	ds_read_b32 v51, v4 offset:5472
	ds_read_b32 v49, v4 offset:5760
	s_waitcnt lgkmcnt(0)
	v_accvgpr_write_b32 a46, v88
	v_mov_b32_e32 v46, v43
	v_accvgpr_write_b32 a8, v8
	v_mov_b32_e32 v113, v61
	v_mov_b32_dpp v46, v61 row_shr:1 row_mask:0xf bank_mask:0xf
	v_accvgpr_mov_b32 a42, a52
	v_accvgpr_write_b32 a47, v89
	v_accvgpr_write_b32 a9, v9
	v_pk_mul_f32 v[88:89], v[112:113], v[46:47]
	v_accvgpr_write_b32 a40, v112
	v_accvgpr_read_b32 v8, a18
	v_accvgpr_read_b32 v113, a39
	v_accvgpr_mov_b32 a43, a53
	v_accvgpr_write_b32 a51, v33
	v_accvgpr_write_b32 a52, v74
	v_accvgpr_read_b32 v9, a19
	v_accvgpr_read_b32 v112, a38
	v_mov_b32_e32 v26, v19
	v_accvgpr_write_b32 a50, v32
	v_accvgpr_write_b32 a53, v75
	v_mov_b32_dpp v43, v60 row_shl:1 row_mask:0xf bank_mask:0xf
	v_pk_fma_f32 v[88:89], v[60:61], v[8:9], v[88:89] op_sel_hi:[0,1,1]
	v_pk_mov_b32 v[60:61], v[60:61], v[112:113] op_sel:[1,0]
	v_mov_b32_dpp v26, v63 row_shr:1 row_mask:0xf bank_mask:0xf
	v_accvgpr_read_b32 v32, a34
	v_mov_b32_e32 v33, v63
	v_accvgpr_read_b32 v127, a27
	v_accvgpr_read_b32 v75, a43
	v_pk_fma_f32 v[60:61], v[60:61], v[42:43], v[88:89]
	v_pk_mul_f32 v[88:89], v[32:33], v[26:27]
	v_accvgpr_read_b32 v126, a26
	v_accvgpr_read_b32 v74, a42
	v_mov_b32_dpp v19, v62 row_shl:1 row_mask:0xf bank_mask:0xf
	v_pk_fma_f32 v[88:89], v[62:63], v[126:127], v[88:89] op_sel_hi:[0,1,1]
	v_pk_mov_b32 v[62:63], v[62:63], v[74:75] op_sel:[1,0]
	v_mov_b32_e32 v44, v39
	v_accvgpr_mov_b32 a14, a48
	v_pk_fma_f32 v[62:63], v[62:63], v[18:19], v[88:89]
	v_pk_add_f32 v[60:61], v[60:61], 0 op_sel_hi:[1,0]
	v_mov_b32_dpp v44, v69 row_shr:1 row_mask:0xf bank_mask:0xf
	v_mov_b32_e32 v1, v69
	v_accvgpr_mov_b32 a15, a49
	v_pk_add_f32 v[60:61], v[60:61], v[62:63]
	v_pk_mul_f32 v[62:63], v[0:1], v[44:45]
	v_accvgpr_write_b32 a48, v0
	v_accvgpr_read_b32 v89, a45
	v_accvgpr_read_b32 v0, a46
	v_accvgpr_read_b32 v88, a44
	v_accvgpr_read_b32 v1, a47
	v_mov_b32_dpp v39, v68 row_shl:1 row_mask:0xf bank_mask:0xf
	v_pk_fma_f32 v[62:63], v[68:69], v[88:89], v[62:63] op_sel_hi:[0,1,1]
	v_pk_mov_b32 v[68:69], v[68:69], v[0:1] op_sel:[1,0]
	v_mov_b32_e32 v36, v25
	v_pk_fma_f32 v[62:63], v[68:69], v[38:39], v[62:63]
	s_mov_b64 s[0:1], 0x800000
	v_pk_add_f32 v[60:61], v[60:61], v[62:63]
	v_mov_b32_dpp v36, v71 row_shr:1 row_mask:0xf bank_mask:0xf
	v_mov_b32_e32 v65, v71
	v_lshl_add_u64 v[62:63], v[54:55], 0, s[0:1]
	v_mov_b32_e32 v128, v60
	v_mov_b32_e32 v129, v61
	v_pk_mul_f32 v[60:61], v[64:65], v[36:37]
	v_mov_b64_e32 v[118:119], v[86:87]
	v_mov_b32_e32 v12, v7
	v_accvgpr_write_b32 a24, v32
	v_mov_b32_dpp v25, v70 row_shl:1 row_mask:0xf bank_mask:0xf
	v_pk_fma_f32 v[60:61], v[70:71], v[118:119], v[60:61] op_sel_hi:[0,1,1]
	v_mov_b32_e32 v62, v71
	v_mov_b32_e32 v63, v113
	v_mov_b32_dpp v12, v73 row_shr:1 row_mask:0xf bank_mask:0xf
	v_accvgpr_read_b32 v32, a20
	v_mov_b32_e32 v33, v73
	v_pk_fma_f32 v[60:61], v[62:63], v[24:25], v[60:61]
	v_pk_mul_f32 v[62:63], v[32:33], v[12:13]
	v_mov_b32_dpp v7, v72 row_shl:1 row_mask:0xf bank_mask:0xf
	v_pk_fma_f32 v[62:63], v[72:73], v[106:107], v[62:63] op_sel_hi:[0,1,1]
	v_mov_b32_e32 v68, v73
	v_mov_b32_e32 v69, v75
	v_mov_b32_e32 v78, v21
	v_pk_fma_f32 v[62:63], v[68:69], v[6:7], v[62:63]
	v_pk_add_f32 v[60:61], v[60:61], 0 op_sel_hi:[1,0]
	v_mov_b32_dpp v78, v83 row_shr:1 row_mask:0xf bank_mask:0xf
	v_mov_b32_e32 v53, v83
	v_pk_add_f32 v[60:61], v[60:61], v[62:63]
	v_pk_mul_f32 v[62:63], v[52:53], v[78:79]
	v_mov_b32_dpp v21, v82 row_shl:1 row_mask:0xf bank_mask:0xf
	v_pk_fma_f32 v[62:63], v[82:83], v[14:15], v[62:63] op_sel_hi:[0,1,1]
	v_mov_b32_e32 v68, v83
	v_mov_b32_e32 v69, v1
	v_accvgpr_write_b32 a19, v15
	v_pk_fma_f32 v[62:63], v[68:69], v[20:21], v[62:63]
	v_mov_b32_e32 v76, v11
	v_accvgpr_write_b32 a18, v14
	v_pk_add_f32 v[60:61], v[60:61], v[62:63]
	s_mov_b64 s[0:1], 0x810000
	v_mov_b32_dpp v76, v81 row_shr:1 row_mask:0xf bank_mask:0xf
	v_mov_b32_e32 v41, v81
	v_accvgpr_read_b32 v14, a36
	v_accvgpr_write_b32 a6, v2
	v_lshl_add_u64 v[136:137], v[134:135], 0, s[0:1]
	s_nop 1
	s_mov_b64 vcc, s[28:29]
	s_nop 0
	v_cndmask_b32_dpp v130, v60, v128, vcc quad_perm:[1,0,3,2] row_mask:0xf bank_mask:0xf
	v_cndmask_b32_dpp v131, v61, v129, vcc quad_perm:[1,0,3,2] row_mask:0xf bank_mask:0xf
	s_mov_b64 vcc, s[30:31]
	s_nop 0
	v_cndmask_b32_dpp v132, v128, v60, vcc quad_perm:[1,0,3,2] row_mask:0xf bank_mask:0xf
	v_cndmask_b32_dpp v133, v129, v61, vcc quad_perm:[1,0,3,2] row_mask:0xf bank_mask:0xf
	global_store_dwordx4 v[136:137], v[130:133], off sc0 sc1 nt
	s_nop 1
	v_pk_mul_f32 v[60:61], v[40:41], v[76:77]
	v_accvgpr_read_b32 v15, a37
	v_mov_b32_e32 v2, v35
	v_mov_b32_dpp v11, v80 row_shl:1 row_mask:0xf bank_mask:0xf
	v_pk_fma_f32 v[60:61], v[80:81], v[14:15], v[60:61] op_sel_hi:[0,1,1]
	v_pk_mov_b32 v[62:63], v[80:81], v[66:67] op_sel:[1,0]
	v_mov_b32_dpp v2, v85 row_shr:1 row_mask:0xf bank_mask:0xf
	v_mov_b32_e32 v23, v85
	v_accvgpr_read_b32 v15, a9
	v_pk_fma_f32 v[60:61], v[62:63], v[10:11], v[60:61]
	v_pk_mul_f32 v[62:63], v[22:23], v[2:3]
	v_accvgpr_read_b32 v14, a8
	v_mov_b32_dpp v35, v84 row_shl:1 row_mask:0xf bank_mask:0xf
	v_pk_fma_f32 v[62:63], v[84:85], v[100:101], v[62:63] op_sel_hi:[0,1,1]
	v_pk_mov_b32 v[68:69], v[84:85], v[14:15] op_sel:[1,0]
	v_mov_b32_e32 v92, v59
	v_pk_fma_f32 v[62:63], v[68:69], v[34:35], v[62:63]
	v_pk_add_f32 v[60:61], v[60:61], 0 op_sel_hi:[1,0]
	v_mov_b32_dpp v92, v125 row_shr:1 row_mask:0xf bank_mask:0xf
	v_mov_b32_e32 v97, v125
	v_accvgpr_read_b32 v71, a15
	v_pk_add_f32 v[60:61], v[60:61], v[62:63]
	v_pk_mul_f32 v[62:63], v[96:97], v[92:93]
	v_accvgpr_read_b32 v70, a14
	v_mov_b32_dpp v59, v124 row_shl:1 row_mask:0xf bank_mask:0xf
	v_pk_fma_f32 v[62:63], v[124:125], v[16:17], v[62:63] op_sel_hi:[0,1,1]
	v_pk_mov_b32 v[68:69], v[124:125], v[70:71] op_sel:[1,0]
	v_mov_b32_e32 v94, v57
	v_pk_fma_f32 v[62:63], v[68:69], v[58:59], v[62:63]
	s_mov_b64 s[0:1], 0x820000
	v_pk_add_f32 v[60:61], v[60:61], v[62:63]
	v_mov_b32_dpp v94, v123 row_shr:1 row_mask:0xf bank_mask:0xf
	v_mov_b32_e32 v99, v123
	v_accvgpr_write_b32 a31, v17
	v_lshl_add_u64 v[62:63], v[54:55], 0, s[0:1]
	v_mov_b32_e32 v128, v60
	v_mov_b32_e32 v129, v61
	v_pk_mul_f32 v[60:61], v[98:99], v[94:95]
	v_mov_b32_e32 v102, v51
	v_accvgpr_write_b32 a30, v16
	v_mov_b32_dpp v57, v122 row_shl:1 row_mask:0xf bank_mask:0xf
	v_pk_fma_f32 v[60:61], v[122:123], v[28:29], v[60:61] op_sel_hi:[0,1,1]
	v_mov_b32_e32 v62, v123
	v_mov_b32_e32 v63, v67
	v_mov_b32_dpp v102, v121 row_shr:1 row_mask:0xf bank_mask:0xf
	v_mov_b32_e32 v105, v121
	v_accvgpr_read_b32 v16, a28
	v_pk_fma_f32 v[60:61], v[62:63], v[56:57], v[60:61]
	v_pk_mul_f32 v[62:63], v[104:105], v[102:103]
	v_accvgpr_read_b32 v17, a29
	v_mov_b32_dpp v51, v120 row_shl:1 row_mask:0xf bank_mask:0xf
	v_pk_fma_f32 v[62:63], v[120:121], v[16:17], v[62:63] op_sel_hi:[0,1,1]
	v_mov_b32_e32 v68, v121
	v_mov_b32_e32 v69, v15
	v_mov_b32_e32 v108, v49
	v_pk_fma_f32 v[62:63], v[68:69], v[50:51], v[62:63]
	v_pk_add_f32 v[60:61], v[60:61], 0 op_sel_hi:[1,0]
	v_mov_b32_dpp v108, v91 row_shr:1 row_mask:0xf bank_mask:0xf
	v_mov_b32_e32 v111, v91
	v_pk_add_f32 v[60:61], v[60:61], v[62:63]
	v_pk_mul_f32 v[62:63], v[110:111], v[108:109]
	v_mov_b32_dpp v49, v90 row_shl:1 row_mask:0xf bank_mask:0xf
	v_pk_fma_f32 v[62:63], v[90:91], v[30:31], v[62:63] op_sel_hi:[0,1,1]
	v_mov_b32_e32 v68, v91
	v_mov_b32_e32 v69, v71
	v_pk_fma_f32 v[62:63], v[68:69], v[48:49], v[62:63]
	s_mov_b64 s[0:1], 0x830000
	v_mov_b32_e32 v0, v22
	v_pk_add_f32 v[60:61], v[60:61], v[62:63]
	v_lshl_add_u64 v[136:137], v[134:135], 0, s[0:1]
	s_add_u32 s0, s10, 0x1c00000
	v_accvgpr_read_b32 v22, a50
	v_accvgpr_read_b32 v1, a72
	s_addc_u32 s1, s11, 0
	v_accvgpr_read_b32 v23, a51
	s_nop 1
	s_mov_b64 vcc, s[28:29]
	s_nop 0
	v_cndmask_b32_dpp v130, v60, v128, vcc quad_perm:[1,0,3,2] row_mask:0xf bank_mask:0xf
	v_cndmask_b32_dpp v131, v61, v129, vcc quad_perm:[1,0,3,2] row_mask:0xf bank_mask:0xf
	s_mov_b64 vcc, s[30:31]
	s_nop 0
	v_cndmask_b32_dpp v132, v128, v60, vcc quad_perm:[1,0,3,2] row_mask:0xf bank_mask:0xf
	v_cndmask_b32_dpp v133, v129, v61, vcc quad_perm:[1,0,3,2] row_mask:0xf bank_mask:0xf
	global_store_dwordx4 v[136:137], v[130:133], off sc0 sc1 nt
	s_nop 1
	v_readfirstlane_b32 s2, v1
	v_lshl_add_u64 v[60:61], s[0:1], 0, v[22:23]
	v_accvgpr_read_b32 v1, a12
	v_accvgpr_read_b32 v22, a52
	s_waitcnt vmcnt(18)
	s_mov_b32 m0, s2
	v_readfirstlane_b32 s2, v1
	v_accvgpr_read_b32 v23, a53
	v_accvgpr_read_b32 v1, a13
	s_waitcnt lgkmcnt(0)
	s_barrier
	global_load_lds_dwordx4 v[60:61], off nt
	v_lshl_add_u64 v[60:61], s[0:1], 0, v[22:23]
	s_mov_b32 m0, s2
	v_readfirstlane_b32 s2, v1
	v_accvgpr_read_b32 v1, a16
	global_load_lds_dwordx4 v[60:61], off nt
	v_lshl_add_u64 v[60:61], s[0:1], 0, v[114:115]
	s_mov_b32 m0, s2
	v_readfirstlane_b32 s2, v1
	global_load_lds_dwordx4 v[60:61], off nt
	v_lshl_add_u64 v[60:61], s[0:1], 0, v[116:117]
	s_mov_b32 m0, s2
	v_accvgpr_write_b32 a22, v30
	v_accvgpr_write_b32 a44, v70
	global_load_lds_dwordx4 v[60:61], off nt
	v_accvgpr_write_b32 a2, v106
	v_accvgpr_write_b32 a34, v74
	v_accvgpr_write_b32 a23, v31
	v_accvgpr_write_b32 a45, v71
	v_add_u32_e32 v2, 0x7010, v5
	v_mov_b32_e32 v31, v5
	v_add_u32_e32 v5, 0x7000, v4
	ds_read_b64 v[60:61], v2
	ds_read_b64 v[62:63], v2 offset:288
	ds_read_b64 v[68:69], v2 offset:576
	ds_read_b64 v[70:71], v2 offset:1728
	ds_read_b64 v[72:73], v2 offset:2016
	ds_read_b64 v[82:83], v2 offset:2304
	ds_read_b64 v[80:81], v2 offset:3456
	ds_read_b64 v[84:85], v2 offset:3744
	ds_read_b64 v[116:117], v2 offset:4032
	ds_read_b64 v[114:115], v2 offset:5184
	ds_read_b64 v[112:113], v2 offset:5472
	ds_read_b64 v[90:91], v2 offset:5760
	ds_read_b32 v43, v5
	ds_read_b32 v19, v5 offset:288
	ds_read_b32 v39, v5 offset:576
	ds_read_b32 v25, v5 offset:1728
	ds_read_b32 v7, v5 offset:2016
	ds_read_b32 v21, v5 offset:2304
	ds_read_b32 v11, v5 offset:3456
	ds_read_b32 v35, v5 offset:3744
	ds_read_b32 v59, v5 offset:4032
	ds_read_b32 v57, v5 offset:5184
	ds_read_b32 v51, v5 offset:5472
	ds_read_b32 v49, v5 offset:5760
	s_waitcnt lgkmcnt(0)
	v_accvgpr_write_b32 a3, v107
	v_mov_b32_e32 v46, v43
	v_accvgpr_write_b32 a35, v75
	v_accvgpr_read_b32 v74, a40
	v_mov_b32_dpp v46, v61 row_shr:1 row_mask:0xf bank_mask:0xf
	v_mov_b32_e32 v75, v61
	v_accvgpr_read_b32 v107, a39
	v_accvgpr_write_b32 a10, v100
	v_pk_mul_f32 v[86:87], v[74:75], v[46:47]
	v_accvgpr_read_b32 v106, a38
	v_mov_b32_e32 v26, v19
	v_accvgpr_write_b32 a11, v101
	v_mov_b32_dpp v43, v60 row_shl:1 row_mask:0xf bank_mask:0xf
	v_mov_b32_e32 v32, v74
	v_pk_fma_f32 v[86:87], v[60:61], v[8:9], v[86:87] op_sel_hi:[0,1,1]
	v_pk_mov_b32 v[60:61], v[60:61], v[106:107] op_sel:[1,0]
	v_mov_b32_dpp v26, v63 row_shr:1 row_mask:0xf bank_mask:0xf
	v_accvgpr_read_b32 v74, a24
	v_mov_b32_e32 v75, v63
	v_accvgpr_read_b32 v101, a35
	v_pk_fma_f32 v[60:61], v[60:61], v[42:43], v[86:87]
	v_pk_mul_f32 v[86:87], v[74:75], v[26:27]
	v_accvgpr_read_b32 v100, a34
	v_accvgpr_write_b32 a14, v66
	v_mov_b32_dpp v19, v62 row_shl:1 row_mask:0xf bank_mask:0xf
	v_pk_fma_f32 v[86:87], v[62:63], v[126:127], v[86:87] op_sel_hi:[0,1,1]
	v_pk_mov_b32 v[62:63], v[62:63], v[100:101] op_sel:[1,0]
	v_mov_b32_e32 v44, v39
	v_accvgpr_write_b32 a42, v64
	v_accvgpr_write_b32 a15, v67
	v_mov_b32_e32 v66, v4
	v_pk_fma_f32 v[62:63], v[62:63], v[18:19], v[86:87]
	v_pk_add_f32 v[60:61], v[60:61], 0 op_sel_hi:[1,0]
	v_mov_b32_dpp v44, v69 row_shr:1 row_mask:0xf bank_mask:0xf
	v_accvgpr_read_b32 v64, a48
	v_mov_b32_e32 v65, v69
	v_accvgpr_read_b32 v4, a46
	v_pk_add_f32 v[60:61], v[60:61], v[62:63]
	v_pk_mul_f32 v[62:63], v[64:65], v[44:45]
	v_accvgpr_read_b32 v5, a47
	v_mov_b32_dpp v39, v68 row_shl:1 row_mask:0xf bank_mask:0xf
	v_pk_fma_f32 v[62:63], v[68:69], v[88:89], v[62:63] op_sel_hi:[0,1,1]
	v_pk_mov_b32 v[68:69], v[68:69], v[4:5] op_sel:[1,0]
	v_mov_b32_e32 v36, v25
	v_pk_fma_f32 v[62:63], v[68:69], v[38:39], v[62:63]
	s_mov_b64 s[0:1], 0xc00000
	v_pk_add_f32 v[60:61], v[60:61], v[62:63]
	v_mov_b32_dpp v36, v71 row_shr:1 row_mask:0xf bank_mask:0xf
	v_accvgpr_read_b32 v22, a42
	v_mov_b32_e32 v23, v71
	v_accvgpr_mov_b32 a26, a20
	v_accvgpr_write_b32 a20, v28
	v_lshl_add_u64 v[62:63], v[54:55], 0, s[0:1]
	v_mov_b32_e32 v128, v60
	v_mov_b32_e32 v129, v61
	v_pk_mul_f32 v[60:61], v[22:23], v[36:37]
	v_mov_b32_e32 v12, v7
	v_accvgpr_write_b32 a21, v29
	v_mov_b32_dpp v25, v70 row_shl:1 row_mask:0xf bank_mask:0xf
	v_pk_fma_f32 v[60:61], v[70:71], v[118:119], v[60:61] op_sel_hi:[0,1,1]
	v_mov_b32_e32 v62, v71
	v_mov_b32_e32 v63, v107
	v_mov_b32_dpp v12, v73 row_shr:1 row_mask:0xf bank_mask:0xf
	v_accvgpr_read_b32 v28, a26
	v_mov_b32_e32 v29, v73
	v_accvgpr_read_b32 v121, a3
	v_pk_fma_f32 v[60:61], v[62:63], v[24:25], v[60:61]
	v_pk_mul_f32 v[62:63], v[28:29], v[12:13]
	v_accvgpr_read_b32 v120, a2
	v_mov_b32_dpp v7, v72 row_shl:1 row_mask:0xf bank_mask:0xf
	v_pk_fma_f32 v[62:63], v[72:73], v[120:121], v[62:63] op_sel_hi:[0,1,1]
	v_mov_b32_e32 v68, v73
	v_mov_b32_e32 v69, v101
	v_mov_b32_e32 v78, v21
	v_pk_fma_f32 v[62:63], v[68:69], v[6:7], v[62:63]
	v_pk_add_f32 v[60:61], v[60:61], 0 op_sel_hi:[1,0]
	v_mov_b32_dpp v78, v83 row_shr:1 row_mask:0xf bank_mask:0xf
	v_mov_b32_e32 v53, v83
	v_accvgpr_read_b32 v125, a19
	v_pk_add_f32 v[60:61], v[60:61], v[62:63]
	v_pk_mul_f32 v[62:63], v[52:53], v[78:79]
	v_accvgpr_read_b32 v124, a18
	v_mov_b32_dpp v21, v82 row_shl:1 row_mask:0xf bank_mask:0xf
	v_pk_fma_f32 v[62:63], v[82:83], v[124:125], v[62:63] op_sel_hi:[0,1,1]
	v_mov_b32_e32 v68, v83
	v_mov_b32_e32 v69, v5
	v_pk_fma_f32 v[62:63], v[68:69], v[20:21], v[62:63]
	v_mov_b32_e32 v76, v11
	v_pk_add_f32 v[60:61], v[60:61], v[62:63]
	s_mov_b64 s[0:1], 0xc10000
	v_mov_b32_dpp v76, v81 row_shr:1 row_mask:0xf bank_mask:0xf
	v_mov_b32_e32 v41, v81
	v_accvgpr_read_b32 v123, a37
	v_accvgpr_read_b32 v4, a14
	v_lshl_add_u64 v[136:137], v[134:135], 0, s[0:1]
	s_nop 1
	s_mov_b64 vcc, s[28:29]
	s_nop 0
	v_cndmask_b32_dpp v130, v60, v128, vcc quad_perm:[1,0,3,2] row_mask:0xf bank_mask:0xf
	v_cndmask_b32_dpp v131, v61, v129, vcc quad_perm:[1,0,3,2] row_mask:0xf bank_mask:0xf
	s_mov_b64 vcc, s[30:31]
	s_nop 0
	v_cndmask_b32_dpp v132, v128, v60, vcc quad_perm:[1,0,3,2] row_mask:0xf bank_mask:0xf
	v_cndmask_b32_dpp v133, v129, v61, vcc quad_perm:[1,0,3,2] row_mask:0xf bank_mask:0xf
	global_store_dwordx4 v[136:137], v[130:133], off sc0 sc1 nt
	s_nop 1
	v_pk_mul_f32 v[60:61], v[40:41], v[76:77]
	v_accvgpr_read_b32 v122, a36
	v_accvgpr_read_b32 v5, a15
	v_mov_b32_e32 v2, v35
	v_accvgpr_mov_b32 a32, a24
	v_accvgpr_write_b32 a24, v22
	v_mov_b64_e32 v[22:23], v[118:119]
	v_mov_b32_dpp v11, v80 row_shl:1 row_mask:0xf bank_mask:0xf
	v_pk_fma_f32 v[60:61], v[80:81], v[122:123], v[60:61] op_sel_hi:[0,1,1]
	v_pk_mov_b32 v[62:63], v[80:81], v[4:5] op_sel:[1,0]
	v_mov_b32_dpp v2, v85 row_shr:1 row_mask:0xf bank_mask:0xf
	v_mov_b32_e32 v106, v0
	v_mov_b32_e32 v107, v85
	v_accvgpr_read_b32 v119, a11
	v_pk_fma_f32 v[60:61], v[62:63], v[10:11], v[60:61]
	v_pk_mul_f32 v[62:63], v[106:107], v[2:3]
	v_accvgpr_read_b32 v118, a10
	v_mov_b64_e32 v[100:101], v[14:15]
	v_mov_b32_dpp v35, v84 row_shl:1 row_mask:0xf bank_mask:0xf
	v_pk_fma_f32 v[62:63], v[84:85], v[118:119], v[62:63] op_sel_hi:[0,1,1]
	v_pk_mov_b32 v[68:69], v[84:85], v[100:101] op_sel:[1,0]
	v_mov_b32_e32 v92, v59
	v_accvgpr_write_b32 a26, v52
	v_mov_b32_e32 v74, v40
	v_pk_fma_f32 v[62:63], v[68:69], v[34:35], v[62:63]
	v_pk_add_f32 v[60:61], v[60:61], 0 op_sel_hi:[1,0]
	v_mov_b32_dpp v92, v117 row_shr:1 row_mask:0xf bank_mask:0xf
	v_mov_b32_e32 v97, v117
	v_accvgpr_read_b32 v41, a31
	v_accvgpr_read_b32 v53, a45
	v_pk_add_f32 v[60:61], v[60:61], v[62:63]
	v_pk_mul_f32 v[62:63], v[96:97], v[92:93]
	v_accvgpr_read_b32 v40, a30
	v_accvgpr_read_b32 v52, a44
	v_mov_b32_dpp v59, v116 row_shl:1 row_mask:0xf bank_mask:0xf
	v_pk_fma_f32 v[62:63], v[116:117], v[40:41], v[62:63] op_sel_hi:[0,1,1]
	v_pk_mov_b32 v[68:69], v[116:117], v[52:53] op_sel:[1,0]
	v_mov_b32_e32 v94, v57
	v_pk_fma_f32 v[62:63], v[68:69], v[58:59], v[62:63]
	s_mov_b64 s[0:1], 0xc20000
	v_pk_add_f32 v[60:61], v[60:61], v[62:63]
	v_mov_b32_dpp v94, v115 row_shr:1 row_mask:0xf bank_mask:0xf
	v_mov_b32_e32 v99, v115
	v_accvgpr_read_b32 v14, a20
	v_lshl_add_u64 v[62:63], v[54:55], 0, s[0:1]
	v_mov_b32_e32 v128, v60
	v_mov_b32_e32 v129, v61
	v_pk_mul_f32 v[60:61], v[98:99], v[94:95]
	v_accvgpr_read_b32 v15, a21
	v_mov_b32_e32 v102, v51
	v_mov_b32_dpp v57, v114 row_shl:1 row_mask:0xf bank_mask:0xf
	v_pk_fma_f32 v[60:61], v[114:115], v[14:15], v[60:61] op_sel_hi:[0,1,1]
	v_mov_b32_e32 v62, v115
	v_mov_b32_e32 v63, v5
	v_mov_b32_dpp v102, v113 row_shr:1 row_mask:0xf bank_mask:0xf
	v_mov_b32_e32 v105, v113
	v_pk_fma_f32 v[60:61], v[62:63], v[56:57], v[60:61]
	v_pk_mul_f32 v[62:63], v[104:105], v[102:103]
	v_accvgpr_write_b32 a8, v8
	v_mov_b32_dpp v51, v112 row_shl:1 row_mask:0xf bank_mask:0xf
	v_pk_fma_f32 v[62:63], v[112:113], v[16:17], v[62:63] op_sel_hi:[0,1,1]
	v_mov_b32_e32 v68, v113
	v_mov_b32_e32 v69, v101
	v_mov_b32_e32 v108, v49
	v_accvgpr_write_b32 a9, v9
	v_pk_fma_f32 v[62:63], v[68:69], v[50:51], v[62:63]
	v_pk_add_f32 v[60:61], v[60:61], 0 op_sel_hi:[1,0]
	v_mov_b32_dpp v108, v91 row_shr:1 row_mask:0xf bank_mask:0xf
	v_mov_b32_e32 v111, v91
	v_accvgpr_read_b32 v8, a22
	v_pk_add_f32 v[60:61], v[60:61], v[62:63]
	v_pk_mul_f32 v[62:63], v[110:111], v[108:109]
	v_accvgpr_read_b32 v9, a23
	v_mov_b32_dpp v49, v90 row_shl:1 row_mask:0xf bank_mask:0xf
	v_pk_fma_f32 v[62:63], v[90:91], v[8:9], v[62:63] op_sel_hi:[0,1,1]
	v_mov_b32_e32 v68, v91
	v_mov_b32_e32 v69, v53
	v_pk_fma_f32 v[62:63], v[68:69], v[48:49], v[62:63]
	s_mov_b64 s[0:1], 0xc30000
	v_pk_add_f32 v[60:61], v[60:61], v[62:63]
	v_lshl_add_u64 v[136:137], v[134:135], 0, s[0:1]
	s_nop 1
	s_mov_b64 vcc, s[28:29]
	s_nop 0
	v_cndmask_b32_dpp v130, v60, v128, vcc quad_perm:[1,0,3,2] row_mask:0xf bank_mask:0xf
	v_cndmask_b32_dpp v131, v61, v129, vcc quad_perm:[1,0,3,2] row_mask:0xf bank_mask:0xf
	s_mov_b64 vcc, s[30:31]
	s_nop 0
	v_cndmask_b32_dpp v132, v128, v60, vcc quad_perm:[1,0,3,2] row_mask:0xf bank_mask:0xf
	v_cndmask_b32_dpp v133, v129, v61, vcc quad_perm:[1,0,3,2] row_mask:0xf bank_mask:0xf
	global_store_dwordx4 v[136:137], v[130:133], off sc0 sc1 nt
	s_nop 1
	s_waitcnt vmcnt(20)
	v_accvgpr_write_b32 a16, v88
	v_accvgpr_write_b32 a10, v100
	s_waitcnt lgkmcnt(0)
	s_barrier
	v_add_u32_e32 v2, 0xe010, v31
	v_add_u32_e32 v5, 0xe000, v66
	ds_read_b64 v[60:61], v2
	ds_read_b64 v[62:63], v2 offset:288
	ds_read_b64 v[68:69], v2 offset:576
	ds_read_b64 v[70:71], v2 offset:1728
	ds_read_b64 v[72:73], v2 offset:2016
	ds_read_b64 v[82:83], v2 offset:2304
	ds_read_b64 v[80:81], v2 offset:3456
	ds_read_b64 v[84:85], v2 offset:3744
	ds_read_b64 v[116:117], v2 offset:4032
	ds_read_b64 v[114:115], v2 offset:5184
	ds_read_b64 v[112:113], v2 offset:5472
	ds_read_b64 v[90:91], v2 offset:5760
	ds_read_b32 v43, v5
	ds_read_b32 v19, v5 offset:288
	ds_read_b32 v39, v5 offset:576
	ds_read_b32 v25, v5 offset:1728
	ds_read_b32 v7, v5 offset:2016
	ds_read_b32 v21, v5 offset:2304
	ds_read_b32 v11, v5 offset:3456
	ds_read_b32 v35, v5 offset:3744
	ds_read_b32 v59, v5 offset:4032
	ds_read_b32 v57, v5 offset:5184
	ds_read_b32 v51, v5 offset:5472
	ds_read_b32 v49, v5 offset:5760
	s_waitcnt lgkmcnt(0)
	v_accvgpr_write_b32 a17, v89
	v_mov_b32_e32 v46, v43
	v_accvgpr_write_b32 a11, v101
	v_mov_b32_e32 v33, v61
	v_mov_b32_dpp v46, v61 row_shr:1 row_mask:0xf bank_mask:0xf
	v_accvgpr_read_b32 v89, a9
	v_accvgpr_read_b32 v101, a39
	v_pk_mul_f32 v[86:87], v[32:33], v[46:47]
	v_accvgpr_read_b32 v88, a8
	v_accvgpr_read_b32 v100, a38
	v_mov_b32_e32 v26, v19
	v_accvgpr_write_b32 a19, v17
	v_mov_b32_dpp v43, v60 row_shl:1 row_mask:0xf bank_mask:0xf
	v_pk_fma_f32 v[86:87], v[60:61], v[88:89], v[86:87] op_sel_hi:[0,1,1]
	v_pk_mov_b32 v[60:61], v[60:61], v[100:101] op_sel:[1,0]
	v_mov_b32_dpp v26, v63 row_shr:1 row_mask:0xf bank_mask:0xf
	v_accvgpr_read_b32 v0, a32
	v_mov_b32_e32 v1, v63
	v_accvgpr_read_b32 v4, a34
	v_accvgpr_write_b32 a18, v16
	v_pk_fma_f32 v[60:61], v[60:61], v[42:43], v[86:87]
	v_pk_mul_f32 v[86:87], v[0:1], v[26:27]
	v_mov_b64_e32 v[16:17], v[126:127]
	v_accvgpr_read_b32 v5, a35
	v_mov_b32_dpp v19, v62 row_shl:1 row_mask:0xf bank_mask:0xf
	v_pk_fma_f32 v[86:87], v[62:63], v[16:17], v[86:87] op_sel_hi:[0,1,1]
	v_pk_mov_b32 v[62:63], v[62:63], v[4:5] op_sel:[1,0]
	v_mov_b32_e32 v44, v39
	v_accvgpr_read_b32 v30, a48
	v_mov_b32_e32 v64, v28
	v_accvgpr_write_b32 a7, v66
	v_pk_fma_f32 v[62:63], v[62:63], v[18:19], v[86:87]
	v_pk_add_f32 v[60:61], v[60:61], 0 op_sel_hi:[1,0]
	v_mov_b32_dpp v44, v69 row_shr:1 row_mask:0xf bank_mask:0xf
	v_mov_b32_e32 v31, v69
	v_accvgpr_read_b32 v29, a17
	v_accvgpr_read_b32 v67, a47
	v_pk_add_f32 v[60:61], v[60:61], v[62:63]
	v_pk_mul_f32 v[62:63], v[30:31], v[44:45]
	v_accvgpr_read_b32 v28, a16
	v_accvgpr_read_b32 v66, a46
	v_mov_b32_dpp v39, v68 row_shl:1 row_mask:0xf bank_mask:0xf
	v_pk_fma_f32 v[62:63], v[68:69], v[28:29], v[62:63] op_sel_hi:[0,1,1]
	v_pk_mov_b32 v[68:69], v[68:69], v[66:67] op_sel:[1,0]
	v_mov_b32_e32 v36, v25
	v_pk_fma_f32 v[62:63], v[68:69], v[38:39], v[62:63]
	s_mov_b64 s[0:1], 0x1000000
	v_pk_add_f32 v[60:61], v[60:61], v[62:63]
	v_mov_b32_dpp v36, v71 row_shr:1 row_mask:0xf bank_mask:0xf
	v_accvgpr_read_b32 v126, a24
	v_mov_b32_e32 v127, v71
	v_lshl_add_u64 v[62:63], v[54:55], 0, s[0:1]
	v_mov_b32_e32 v128, v60
	v_mov_b32_e32 v129, v61
	v_pk_mul_f32 v[60:61], v[126:127], v[36:37]
	v_mov_b32_e32 v12, v7
	v_mov_b32_dpp v25, v70 row_shl:1 row_mask:0xf bank_mask:0xf
	v_pk_fma_f32 v[60:61], v[70:71], v[22:23], v[60:61] op_sel_hi:[0,1,1]
	v_mov_b32_e32 v62, v71
	v_mov_b32_e32 v63, v101
	v_mov_b32_dpp v12, v73 row_shr:1 row_mask:0xf bank_mask:0xf
	v_mov_b32_e32 v52, v64
	v_mov_b32_e32 v53, v73
	v_pk_fma_f32 v[60:61], v[62:63], v[24:25], v[60:61]
	v_pk_mul_f32 v[62:63], v[52:53], v[12:13]
	v_mov_b32_dpp v7, v72 row_shl:1 row_mask:0xf bank_mask:0xf
	v_pk_fma_f32 v[62:63], v[72:73], v[120:121], v[62:63] op_sel_hi:[0,1,1]
	v_mov_b32_e32 v68, v73
	v_mov_b32_e32 v69, v5
	v_mov_b32_e32 v78, v21
	v_pk_fma_f32 v[62:63], v[68:69], v[6:7], v[62:63]
	v_pk_add_f32 v[60:61], v[60:61], 0 op_sel_hi:[1,0]
	v_mov_b32_dpp v78, v83 row_shr:1 row_mask:0xf bank_mask:0xf
	v_accvgpr_read_b32 v4, a26
	v_mov_b32_e32 v5, v83
	v_pk_add_f32 v[60:61], v[60:61], v[62:63]
	v_pk_mul_f32 v[62:63], v[4:5], v[78:79]
	v_mov_b32_dpp v21, v82 row_shl:1 row_mask:0xf bank_mask:0xf
	v_pk_fma_f32 v[62:63], v[82:83], v[124:125], v[62:63] op_sel_hi:[0,1,1]
	v_mov_b32_e32 v68, v83
	v_mov_b32_e32 v69, v67
	v_accvgpr_write_b32 a8, v120
	v_pk_fma_f32 v[62:63], v[68:69], v[20:21], v[62:63]
	v_mov_b32_e32 v76, v11
	v_accvgpr_write_b32 a9, v121
	v_pk_add_f32 v[60:61], v[60:61], v[62:63]
	s_mov_b64 s[0:1], 0x1010000
	v_mov_b32_dpp v76, v81 row_shr:1 row_mask:0xf bank_mask:0xf
	v_mov_b32_e32 v120, v74
	v_mov_b32_e32 v121, v81
	v_accvgpr_read_b32 v101, a15
	v_accvgpr_mov_b32 a12, a38
	v_lshl_add_u64 v[136:137], v[134:135], 0, s[0:1]
	s_nop 1
	s_mov_b64 vcc, s[28:29]
	s_nop 0
	v_cndmask_b32_dpp v130, v60, v128, vcc quad_perm:[1,0,3,2] row_mask:0xf bank_mask:0xf
	v_cndmask_b32_dpp v131, v61, v129, vcc quad_perm:[1,0,3,2] row_mask:0xf bank_mask:0xf
	s_mov_b64 vcc, s[30:31]
	s_nop 0
	v_cndmask_b32_dpp v132, v128, v60, vcc quad_perm:[1,0,3,2] row_mask:0xf bank_mask:0xf
	v_cndmask_b32_dpp v133, v129, v61, vcc quad_perm:[1,0,3,2] row_mask:0xf bank_mask:0xf
	global_store_dwordx4 v[136:137], v[130:133], off sc0 sc1 nt
	s_nop 1
	v_pk_mul_f32 v[60:61], v[120:121], v[76:77]
	v_accvgpr_read_b32 v100, a14
	v_mov_b32_e32 v2, v35
	v_accvgpr_mov_b32 a13, a39
	v_accvgpr_write_b32 a20, v22
	v_mov_b32_dpp v11, v80 row_shl:1 row_mask:0xf bank_mask:0xf
	v_pk_fma_f32 v[60:61], v[80:81], v[122:123], v[60:61] op_sel_hi:[0,1,1]
	v_pk_mov_b32 v[62:63], v[80:81], v[100:101] op_sel:[1,0]
	v_mov_b32_dpp v2, v85 row_shr:1 row_mask:0xf bank_mask:0xf
	v_mov_b32_e32 v107, v85
	v_accvgpr_read_b32 v123, a11
	v_accvgpr_write_b32 a21, v23
	v_accvgpr_read_b32 v23, a13
	v_pk_fma_f32 v[60:61], v[62:63], v[10:11], v[60:61]
	v_pk_mul_f32 v[62:63], v[106:107], v[2:3]
	v_accvgpr_read_b32 v122, a10
	v_accvgpr_read_b32 v22, a12
	v_mov_b32_dpp v35, v84 row_shl:1 row_mask:0xf bank_mask:0xf
	v_pk_fma_f32 v[62:63], v[84:85], v[118:119], v[62:63] op_sel_hi:[0,1,1]
	v_accvgpr_write_b32 a12, v118
	v_pk_mov_b32 v[68:69], v[84:85], v[122:123] op_sel:[1,0]
	v_mov_b32_e32 v92, v59
	v_accvgpr_write_b32 a13, v119
	v_pk_fma_f32 v[62:63], v[68:69], v[34:35], v[62:63]
	v_pk_add_f32 v[60:61], v[60:61], 0 op_sel_hi:[1,0]
	v_mov_b32_dpp v92, v117 row_shr:1 row_mask:0xf bank_mask:0xf
	v_mov_b32_e32 v97, v117
	v_mov_b64_e32 v[118:119], v[40:41]
	v_accvgpr_read_b32 v40, a44
	v_pk_add_f32 v[60:61], v[60:61], v[62:63]
	v_pk_mul_f32 v[62:63], v[96:97], v[92:93]
	v_accvgpr_read_b32 v41, a45
	v_mov_b32_dpp v59, v116 row_shl:1 row_mask:0xf bank_mask:0xf
	v_pk_fma_f32 v[62:63], v[116:117], v[118:119], v[62:63] op_sel_hi:[0,1,1]
	v_pk_mov_b32 v[68:69], v[116:117], v[40:41] op_sel:[1,0]
	v_mov_b32_e32 v94, v57
	v_pk_fma_f32 v[62:63], v[68:69], v[58:59], v[62:63]
	s_mov_b64 s[0:1], 0x1020000
	v_pk_add_f32 v[60:61], v[60:61], v[62:63]
	v_mov_b32_dpp v94, v115 row_shr:1 row_mask:0xf bank_mask:0xf
	v_mov_b32_e32 v99, v115
	v_lshl_add_u64 v[62:63], v[54:55], 0, s[0:1]
	v_mov_b32_e32 v128, v60
	v_mov_b32_e32 v129, v61
	v_pk_mul_f32 v[60:61], v[98:99], v[94:95]
	v_mov_b32_e32 v102, v51
	v_accvgpr_write_b32 a30, v4
	v_mov_b32_dpp v57, v114 row_shl:1 row_mask:0xf bank_mask:0xf
	v_pk_fma_f32 v[60:61], v[114:115], v[14:15], v[60:61] op_sel_hi:[0,1,1]
	v_mov_b32_e32 v62, v115
	v_mov_b32_e32 v63, v101
	v_mov_b32_dpp v102, v113 row_shr:1 row_mask:0xf bank_mask:0xf
	v_mov_b32_e32 v105, v113
	v_accvgpr_read_b32 v4, a18
	v_pk_fma_f32 v[60:61], v[62:63], v[56:57], v[60:61]
	v_pk_mul_f32 v[62:63], v[104:105], v[102:103]
	v_accvgpr_read_b32 v5, a19
	v_mov_b32_dpp v51, v112 row_shl:1 row_mask:0xf bank_mask:0xf
	v_pk_fma_f32 v[62:63], v[112:113], v[4:5], v[62:63] op_sel_hi:[0,1,1]
	v_mov_b32_e32 v68, v113
	v_mov_b32_e32 v69, v123
	v_mov_b32_e32 v108, v49
	v_pk_fma_f32 v[62:63], v[68:69], v[50:51], v[62:63]
	v_pk_add_f32 v[60:61], v[60:61], 0 op_sel_hi:[1,0]
	v_mov_b32_dpp v108, v91 row_shr:1 row_mask:0xf bank_mask:0xf
	v_mov_b32_e32 v111, v91
	v_pk_add_f32 v[60:61], v[60:61], v[62:63]
	v_pk_mul_f32 v[62:63], v[110:111], v[108:109]
	v_mov_b32_dpp v49, v90 row_shl:1 row_mask:0xf bank_mask:0xf
	v_pk_fma_f32 v[62:63], v[90:91], v[8:9], v[62:63] op_sel_hi:[0,1,1]
	v_mov_b32_e32 v68, v91
	v_mov_b32_e32 v69, v41
	v_pk_fma_f32 v[62:63], v[68:69], v[48:49], v[62:63]
	s_mov_b64 s[0:1], 0x1030000
	v_pk_add_f32 v[60:61], v[60:61], v[62:63]
	v_lshl_add_u64 v[136:137], v[134:135], 0, s[0:1]
	s_nop 1
	s_mov_b64 vcc, s[28:29]
	s_nop 0
	v_cndmask_b32_dpp v130, v60, v128, vcc quad_perm:[1,0,3,2] row_mask:0xf bank_mask:0xf
	v_cndmask_b32_dpp v131, v61, v129, vcc quad_perm:[1,0,3,2] row_mask:0xf bank_mask:0xf
	s_mov_b64 vcc, s[30:31]
	s_nop 0
	v_cndmask_b32_dpp v132, v128, v60, vcc quad_perm:[1,0,3,2] row_mask:0xf bank_mask:0xf
	v_cndmask_b32_dpp v133, v129, v61, vcc quad_perm:[1,0,3,2] row_mask:0xf bank_mask:0xf
	global_store_dwordx4 v[136:137], v[130:133], off sc0 sc1 nt
	s_nop 1
	s_waitcnt vmcnt(16)
	s_waitcnt lgkmcnt(0)
	s_barrier
	v_accvgpr_read_b32 v2, a0
	v_accvgpr_read_b32 v8, a4
	ds_read_b64 v[60:61], v8
	ds_read_b64 v[62:63], v8 offset:288
	ds_read_b64 v[68:69], v8 offset:576
	ds_read_b64 v[70:71], v8 offset:1728
	ds_read_b64 v[72:73], v8 offset:2016
	ds_read_b64 v[82:83], v8 offset:2304
	ds_read_b64 v[80:81], v8 offset:3456
	ds_read_b64 v[84:85], v8 offset:3744
	ds_read_b64 v[116:117], v8 offset:4032
	ds_read_b64 v[114:115], v8 offset:5184
	ds_read_b64 v[112:113], v8 offset:5472
	ds_read_b64 v[90:91], v8 offset:5760
	ds_read_b32 v43, v2
	ds_read_b32 v19, v2 offset:288
	ds_read_b32 v39, v2 offset:576
	ds_read_b32 v25, v2 offset:1728
	ds_read_b32 v7, v2 offset:2016
	ds_read_b32 v21, v2 offset:2304
	ds_read_b32 v11, v2 offset:3456
	ds_read_b32 v35, v2 offset:3744
	ds_read_b32 v59, v2 offset:4032
	ds_read_b32 v57, v2 offset:5184
	ds_read_b32 v51, v2 offset:5472
	ds_read_b32 v49, v2 offset:5760
	s_waitcnt lgkmcnt(0)
	v_mov_b32_e32 v64, v32
	v_mov_b32_e32 v46, v43
	v_mov_b32_e32 v65, v61
	v_mov_b64_e32 v[100:101], v[22:23]
	v_mov_b32_dpp v46, v61 row_shr:1 row_mask:0xf bank_mask:0xf
	v_pk_mul_f32 v[86:87], v[64:65], v[46:47]
	v_mov_b32_e32 v26, v19
	v_mov_b32_dpp v43, v60 row_shl:1 row_mask:0xf bank_mask:0xf
	v_pk_fma_f32 v[86:87], v[60:61], v[88:89], v[86:87] op_sel_hi:[0,1,1]
	v_pk_mov_b32 v[60:61], v[60:61], v[100:101] op_sel:[1,0]
	v_mov_b32_dpp v26, v63 row_shr:1 row_mask:0xf bank_mask:0xf
	v_mov_b32_e32 v1, v63
	v_accvgpr_read_b32 v67, a35
	v_pk_fma_f32 v[60:61], v[60:61], v[42:43], v[86:87]
	v_pk_mul_f32 v[86:87], v[0:1], v[26:27]
	v_accvgpr_read_b32 v66, a34
	v_accvgpr_write_b32 a10, v14
	v_mov_b32_dpp v19, v62 row_shl:1 row_mask:0xf bank_mask:0xf
	v_pk_fma_f32 v[86:87], v[62:63], v[16:17], v[86:87] op_sel_hi:[0,1,1]
	v_pk_mov_b32 v[62:63], v[62:63], v[66:67] op_sel:[1,0]
	v_mov_b32_e32 v44, v39
	v_accvgpr_write_b32 a11, v15
	v_pk_fma_f32 v[62:63], v[62:63], v[18:19], v[86:87]
	v_pk_add_f32 v[60:61], v[60:61], 0 op_sel_hi:[1,0]
	v_mov_b32_dpp v44, v69 row_shr:1 row_mask:0xf bank_mask:0xf
	v_mov_b32_e32 v31, v69
	v_accvgpr_read_b32 v14, a16
	v_accvgpr_read_b32 v28, a46
	v_pk_add_f32 v[60:61], v[60:61], v[62:63]
	v_pk_mul_f32 v[62:63], v[30:31], v[44:45]
	v_accvgpr_read_b32 v15, a17
	v_accvgpr_read_b32 v29, a47
	v_mov_b32_dpp v39, v68 row_shl:1 row_mask:0xf bank_mask:0xf
	v_pk_fma_f32 v[62:63], v[68:69], v[14:15], v[62:63] op_sel_hi:[0,1,1]
	v_pk_mov_b32 v[68:69], v[68:69], v[28:29] op_sel:[1,0]
	v_mov_b32_e32 v36, v25
	v_pk_fma_f32 v[62:63], v[68:69], v[38:39], v[62:63]
	s_mov_b64 s[0:1], 0x1400000
	v_pk_add_f32 v[60:61], v[60:61], v[62:63]
	v_mov_b32_dpp v36, v71 row_shr:1 row_mask:0xf bank_mask:0xf
	v_mov_b32_e32 v127, v71
	v_accvgpr_read_b32 v8, a20
	v_lshl_add_u64 v[62:63], v[54:55], 0, s[0:1]
	v_mov_b32_e32 v128, v60
	v_mov_b32_e32 v129, v61
	v_pk_mul_f32 v[60:61], v[126:127], v[36:37]
	v_accvgpr_read_b32 v9, a21
	v_accvgpr_write_b32 a25, v23
	v_mov_b32_e32 v12, v7
	v_mov_b32_dpp v25, v70 row_shl:1 row_mask:0xf bank_mask:0xf
	v_pk_fma_f32 v[60:61], v[70:71], v[8:9], v[60:61] op_sel_hi:[0,1,1]
	v_mov_b32_e32 v62, v71
	v_mov_b32_e32 v63, v101
	v_accvgpr_write_b32 a24, v22
	v_mov_b32_dpp v12, v73 row_shr:1 row_mask:0xf bank_mask:0xf
	v_mov_b32_e32 v74, v52
	v_mov_b32_e32 v75, v73
	v_accvgpr_read_b32 v23, a9
	v_accvgpr_write_b32 a26, v124
	v_accvgpr_mov_b32 a2, a22
	v_pk_fma_f32 v[60:61], v[62:63], v[24:25], v[60:61]
	v_pk_mul_f32 v[62:63], v[74:75], v[12:13]
	v_accvgpr_read_b32 v22, a8
	v_accvgpr_write_b32 a27, v125
	v_accvgpr_mov_b32 a3, a23
	v_accvgpr_write_b32 a22, v88
	v_mov_b32_dpp v7, v72 row_shl:1 row_mask:0xf bank_mask:0xf
	v_pk_fma_f32 v[62:63], v[72:73], v[22:23], v[62:63] op_sel_hi:[0,1,1]
	v_mov_b32_e32 v68, v73
	v_mov_b32_e32 v69, v67
	v_mov_b32_e32 v78, v21
	v_accvgpr_write_b32 a23, v89
	v_pk_fma_f32 v[62:63], v[68:69], v[6:7], v[62:63]
	v_pk_add_f32 v[60:61], v[60:61], 0 op_sel_hi:[1,0]
	v_mov_b32_dpp v78, v83 row_shr:1 row_mask:0xf bank_mask:0xf
	v_accvgpr_read_b32 v52, a30
	v_mov_b32_e32 v53, v83
	v_accvgpr_read_b32 v89, a27
	v_pk_add_f32 v[60:61], v[60:61], v[62:63]
	v_pk_mul_f32 v[62:63], v[52:53], v[78:79]
	v_accvgpr_read_b32 v88, a26
	v_mov_b32_dpp v21, v82 row_shl:1 row_mask:0xf bank_mask:0xf
	v_pk_fma_f32 v[62:63], v[82:83], v[88:89], v[62:63] op_sel_hi:[0,1,1]
	v_mov_b32_e32 v68, v83
	v_mov_b32_e32 v69, v29
	v_pk_fma_f32 v[62:63], v[68:69], v[20:21], v[62:63]
	v_mov_b32_e32 v76, v11
	v_accvgpr_read_b32 v125, a37
	v_pk_add_f32 v[60:61], v[60:61], v[62:63]
	s_mov_b64 s[0:1], 0x1410000
	v_mov_b32_dpp v76, v81 row_shr:1 row_mask:0xf bank_mask:0xf
	v_mov_b32_e32 v121, v81
	v_accvgpr_read_b32 v101, a15
	v_accvgpr_read_b32 v124, a36
	v_lshl_add_u64 v[136:137], v[134:135], 0, s[0:1]
	s_nop 1
	s_mov_b64 vcc, s[28:29]
	s_nop 0
	v_cndmask_b32_dpp v130, v60, v128, vcc quad_perm:[1,0,3,2] row_mask:0xf bank_mask:0xf
	v_cndmask_b32_dpp v131, v61, v129, vcc quad_perm:[1,0,3,2] row_mask:0xf bank_mask:0xf
	s_mov_b64 vcc, s[30:31]
	s_nop 0
	v_cndmask_b32_dpp v132, v128, v60, vcc quad_perm:[1,0,3,2] row_mask:0xf bank_mask:0xf
	v_cndmask_b32_dpp v133, v129, v61, vcc quad_perm:[1,0,3,2] row_mask:0xf bank_mask:0xf
	global_store_dwordx4 v[136:137], v[130:133], off sc0 sc1 nt
	s_nop 1
	v_pk_mul_f32 v[60:61], v[120:121], v[76:77]
	v_accvgpr_read_b32 v100, a14
	v_mov_b32_e32 v2, v35
	v_mov_b32_dpp v11, v80 row_shl:1 row_mask:0xf bank_mask:0xf
	v_pk_fma_f32 v[60:61], v[80:81], v[124:125], v[60:61] op_sel_hi:[0,1,1]
	v_pk_mov_b32 v[62:63], v[80:81], v[100:101] op_sel:[1,0]
	v_mov_b32_dpp v2, v85 row_shr:1 row_mask:0xf bank_mask:0xf
	v_mov_b32_e32 v107, v85
	v_accvgpr_read_b32 v29, a13
	v_pk_fma_f32 v[60:61], v[62:63], v[10:11], v[60:61]
	v_pk_mul_f32 v[62:63], v[106:107], v[2:3]
	v_accvgpr_read_b32 v28, a12
	v_mov_b32_dpp v35, v84 row_shl:1 row_mask:0xf bank_mask:0xf
	v_pk_fma_f32 v[62:63], v[84:85], v[28:29], v[62:63] op_sel_hi:[0,1,1]
	v_pk_mov_b32 v[68:69], v[84:85], v[122:123] op_sel:[1,0]
	v_mov_b32_e32 v92, v59
	v_pk_fma_f32 v[62:63], v[68:69], v[34:35], v[62:63]
	v_pk_add_f32 v[60:61], v[60:61], 0 op_sel_hi:[1,0]
	v_mov_b32_dpp v92, v117 row_shr:1 row_mask:0xf bank_mask:0xf
	v_mov_b32_e32 v97, v117
	v_pk_add_f32 v[60:61], v[60:61], v[62:63]
	v_pk_mul_f32 v[62:63], v[96:97], v[92:93]
	v_accvgpr_write_b32 a8, v118
	v_pk_fma_f32 v[62:63], v[116:117], v[118:119], v[62:63] op_sel_hi:[0,1,1]
	v_accvgpr_write_b32 a9, v119
	v_accvgpr_read_b32 v119, a45
	v_accvgpr_read_b32 v118, a44
	v_mov_b32_dpp v59, v116 row_shl:1 row_mask:0xf bank_mask:0xf
	v_pk_mov_b32 v[68:69], v[116:117], v[118:119] op_sel:[1,0]
	v_mov_b32_e32 v94, v57
	v_pk_fma_f32 v[62:63], v[68:69], v[58:59], v[62:63]
	s_mov_b64 s[0:1], 0x1420000
	v_pk_add_f32 v[60:61], v[60:61], v[62:63]
	v_mov_b32_dpp v94, v115 row_shr:1 row_mask:0xf bank_mask:0xf
	v_mov_b32_e32 v99, v115
	v_accvgpr_read_b32 v41, a11
	v_lshl_add_u64 v[62:63], v[54:55], 0, s[0:1]
	v_mov_b32_e32 v128, v60
	v_mov_b32_e32 v129, v61
	v_pk_mul_f32 v[60:61], v[98:99], v[94:95]
	v_accvgpr_read_b32 v40, a10
	v_mov_b32_e32 v102, v51
	v_mov_b32_dpp v57, v114 row_shl:1 row_mask:0xf bank_mask:0xf
	v_pk_fma_f32 v[60:61], v[114:115], v[40:41], v[60:61] op_sel_hi:[0,1,1]
	v_mov_b32_e32 v62, v115
	v_mov_b32_e32 v63, v101
	v_mov_b32_dpp v102, v113 row_shr:1 row_mask:0xf bank_mask:0xf
	v_mov_b32_e32 v105, v113
	v_pk_fma_f32 v[60:61], v[62:63], v[56:57], v[60:61]
	v_pk_mul_f32 v[62:63], v[104:105], v[102:103]
	v_mov_b32_dpp v51, v112 row_shl:1 row_mask:0xf bank_mask:0xf
	v_pk_fma_f32 v[62:63], v[112:113], v[4:5], v[62:63] op_sel_hi:[0,1,1]
	v_mov_b32_e32 v68, v113
	v_mov_b32_e32 v69, v123
	v_mov_b32_e32 v108, v49
	v_pk_fma_f32 v[62:63], v[68:69], v[50:51], v[62:63]
	v_pk_add_f32 v[60:61], v[60:61], 0 op_sel_hi:[1,0]
	v_mov_b32_dpp v108, v91 row_shr:1 row_mask:0xf bank_mask:0xf
	v_mov_b32_e32 v111, v91
	v_accvgpr_read_b32 v5, a3
	v_pk_add_f32 v[60:61], v[60:61], v[62:63]
	v_pk_mul_f32 v[62:63], v[110:111], v[108:109]
	v_accvgpr_read_b32 v4, a2
	v_mov_b32_dpp v49, v90 row_shl:1 row_mask:0xf bank_mask:0xf
	v_pk_fma_f32 v[62:63], v[90:91], v[4:5], v[62:63] op_sel_hi:[0,1,1]
	v_mov_b32_e32 v68, v91
	v_mov_b32_e32 v69, v119
	v_pk_fma_f32 v[62:63], v[68:69], v[48:49], v[62:63]
	s_mov_b64 s[0:1], 0x1430000
	v_pk_add_f32 v[60:61], v[60:61], v[62:63]
	v_lshl_add_u64 v[136:137], v[134:135], 0, s[0:1]
	s_nop 1
	s_mov_b64 vcc, s[28:29]
	s_nop 0
	v_cndmask_b32_dpp v130, v60, v128, vcc quad_perm:[1,0,3,2] row_mask:0xf bank_mask:0xf
	v_cndmask_b32_dpp v131, v61, v129, vcc quad_perm:[1,0,3,2] row_mask:0xf bank_mask:0xf
	s_mov_b64 vcc, s[30:31]
	s_nop 0
	v_cndmask_b32_dpp v132, v128, v60, vcc quad_perm:[1,0,3,2] row_mask:0xf bank_mask:0xf
	v_cndmask_b32_dpp v133, v129, v61, vcc quad_perm:[1,0,3,2] row_mask:0xf bank_mask:0xf
	global_store_dwordx4 v[136:137], v[130:133], off sc0 sc1 nt
	s_nop 1
	s_waitcnt vmcnt(12)
	s_waitcnt lgkmcnt(0)
	s_barrier
	v_accvgpr_read_b32 v2, a1
	v_accvgpr_read_b32 v12, a5
	ds_read_b64 v[60:61], v12
	ds_read_b64 v[62:63], v12 offset:288
	ds_read_b64 v[68:69], v12 offset:576
	ds_read_b64 v[70:71], v12 offset:1728
	ds_read_b64 v[72:73], v12 offset:2016
	ds_read_b64 v[82:83], v12 offset:2304
	ds_read_b64 v[80:81], v12 offset:3456
	ds_read_b64 v[84:85], v12 offset:3744
	ds_read_b64 v[116:117], v12 offset:4032
	ds_read_b64 v[114:115], v12 offset:5184
	ds_read_b64 v[112:113], v12 offset:5472
	ds_read_b64 v[90:91], v12 offset:5760
	ds_read_b32 v43, v2
	ds_read_b32 v19, v2 offset:288
	ds_read_b32 v39, v2 offset:576
	ds_read_b32 v25, v2 offset:1728
	ds_read_b32 v7, v2 offset:2016
	ds_read_b32 v21, v2 offset:2304
	ds_read_b32 v11, v2 offset:3456
	ds_read_b32 v35, v2 offset:3744
	ds_read_b32 v59, v2 offset:4032
	ds_read_b32 v57, v2 offset:5184
	ds_read_b32 v51, v2 offset:5472
	ds_read_b32 v49, v2 offset:5760
	s_waitcnt lgkmcnt(0)
	v_accvgpr_read_b32 v101, a23
	v_mov_b32_e32 v46, v43
	v_mov_b32_e32 v65, v61
	v_accvgpr_read_b32 v31, a25
	v_mov_b32_dpp v46, v61 row_shr:1 row_mask:0xf bank_mask:0xf
	v_pk_mul_f32 v[86:87], v[64:65], v[46:47]
	v_accvgpr_read_b32 v100, a22
	v_accvgpr_read_b32 v30, a24
	v_mov_b32_e32 v26, v19
	v_mov_b32_dpp v43, v60 row_shl:1 row_mask:0xf bank_mask:0xf
	v_pk_fma_f32 v[86:87], v[60:61], v[100:101], v[86:87] op_sel_hi:[0,1,1]
	v_pk_mov_b32 v[60:61], v[60:61], v[30:31] op_sel:[1,0]
	v_mov_b32_dpp v26, v63 row_shr:1 row_mask:0xf bank_mask:0xf
	v_mov_b32_e32 v1, v63
	v_pk_fma_f32 v[60:61], v[60:61], v[42:43], v[86:87]
	v_pk_mul_f32 v[86:87], v[0:1], v[26:27]
	v_accvgpr_read_b32 v0, a34
	v_accvgpr_mov_b32 a12, a14
	v_accvgpr_read_b32 v1, a35
	v_accvgpr_mov_b32 a13, a15
	v_mov_b32_dpp v19, v62 row_shl:1 row_mask:0xf bank_mask:0xf
	v_pk_fma_f32 v[86:87], v[62:63], v[16:17], v[86:87] op_sel_hi:[0,1,1]
	v_accvgpr_write_b32 a14, v16
	v_pk_mov_b32 v[62:63], v[62:63], v[0:1] op_sel:[1,0]
	v_mov_b32_e32 v44, v39
	v_accvgpr_write_b32 a15, v17
	v_pk_fma_f32 v[62:63], v[62:63], v[18:19], v[86:87]
	v_pk_add_f32 v[60:61], v[60:61], 0 op_sel_hi:[1,0]
	v_mov_b32_dpp v44, v69 row_shr:1 row_mask:0xf bank_mask:0xf
	v_accvgpr_read_b32 v16, a48
	v_mov_b32_e32 v17, v69
	v_accvgpr_read_b32 v67, a47
	v_pk_add_f32 v[60:61], v[60:61], v[62:63]
	v_pk_mul_f32 v[62:63], v[16:17], v[44:45]
	v_accvgpr_read_b32 v66, a46
	v_mov_b32_dpp v39, v68 row_shl:1 row_mask:0xf bank_mask:0xf
	v_pk_fma_f32 v[62:63], v[68:69], v[14:15], v[62:63] op_sel_hi:[0,1,1]
	v_pk_mov_b32 v[68:69], v[68:69], v[66:67] op_sel:[1,0]
	v_mov_b32_e32 v36, v25
	v_pk_fma_f32 v[62:63], v[68:69], v[38:39], v[62:63]
	s_mov_b64 s[0:1], 0x1800000
	v_pk_add_f32 v[60:61], v[60:61], v[62:63]
	v_mov_b32_dpp v36, v71 row_shr:1 row_mask:0xf bank_mask:0xf
	v_mov_b32_e32 v127, v71
	v_lshl_add_u64 v[62:63], v[54:55], 0, s[0:1]
	v_mov_b32_e32 v128, v60
	v_mov_b32_e32 v129, v61
	v_pk_mul_f32 v[60:61], v[126:127], v[36:37]
	v_mov_b32_e32 v12, v7
	v_mov_b32_dpp v25, v70 row_shl:1 row_mask:0xf bank_mask:0xf
	v_pk_fma_f32 v[60:61], v[70:71], v[8:9], v[60:61] op_sel_hi:[0,1,1]
	v_mov_b32_e32 v62, v71
	v_mov_b32_e32 v63, v31
	v_mov_b32_dpp v12, v73 row_shr:1 row_mask:0xf bank_mask:0xf
	v_mov_b32_e32 v75, v73
	v_pk_fma_f32 v[60:61], v[62:63], v[24:25], v[60:61]
	v_pk_mul_f32 v[62:63], v[74:75], v[12:13]
	v_mov_b32_dpp v7, v72 row_shl:1 row_mask:0xf bank_mask:0xf
	v_pk_fma_f32 v[62:63], v[72:73], v[22:23], v[62:63] op_sel_hi:[0,1,1]
	v_accvgpr_write_b32 a4, v22
	v_mov_b32_e32 v68, v73
	v_mov_b32_e32 v69, v1
	v_mov_b32_e32 v78, v21
	v_accvgpr_write_b32 a5, v23
	v_pk_fma_f32 v[62:63], v[68:69], v[6:7], v[62:63]
	v_pk_add_f32 v[60:61], v[60:61], 0 op_sel_hi:[1,0]
	v_mov_b32_dpp v78, v83 row_shr:1 row_mask:0xf bank_mask:0xf
	v_mov_b32_e32 v53, v83
	v_accvgpr_read_b32 v22, a26
	v_pk_add_f32 v[60:61], v[60:61], v[62:63]
	v_pk_mul_f32 v[62:63], v[52:53], v[78:79]
	v_accvgpr_read_b32 v23, a27
	v_mov_b32_dpp v21, v82 row_shl:1 row_mask:0xf bank_mask:0xf
	v_pk_fma_f32 v[62:63], v[82:83], v[22:23], v[62:63] op_sel_hi:[0,1,1]
	v_mov_b32_e32 v68, v83
	v_mov_b32_e32 v69, v67
	v_pk_fma_f32 v[62:63], v[68:69], v[20:21], v[62:63]
	v_mov_b32_e32 v76, v11
	v_pk_add_f32 v[60:61], v[60:61], v[62:63]
	s_mov_b64 s[0:1], 0x1810000
	v_mov_b32_dpp v76, v81 row_shr:1 row_mask:0xf bank_mask:0xf
	v_mov_b32_e32 v121, v81
	v_accvgpr_read_b32 v15, a13
	v_lshl_add_u64 v[136:137], v[134:135], 0, s[0:1]
	s_nop 1
	s_mov_b64 vcc, s[28:29]
	s_nop 0
	v_cndmask_b32_dpp v130, v60, v128, vcc quad_perm:[1,0,3,2] row_mask:0xf bank_mask:0xf
	v_cndmask_b32_dpp v131, v61, v129, vcc quad_perm:[1,0,3,2] row_mask:0xf bank_mask:0xf
	s_mov_b64 vcc, s[30:31]
	s_nop 0
	v_cndmask_b32_dpp v132, v128, v60, vcc quad_perm:[1,0,3,2] row_mask:0xf bank_mask:0xf
	v_cndmask_b32_dpp v133, v129, v61, vcc quad_perm:[1,0,3,2] row_mask:0xf bank_mask:0xf
	global_store_dwordx4 v[136:137], v[130:133], off sc0 sc1 nt
	s_nop 1
	v_pk_mul_f32 v[60:61], v[120:121], v[76:77]
	v_accvgpr_read_b32 v14, a12
	v_mov_b32_e32 v2, v35
	v_mov_b32_dpp v11, v80 row_shl:1 row_mask:0xf bank_mask:0xf
	v_pk_fma_f32 v[60:61], v[80:81], v[124:125], v[60:61] op_sel_hi:[0,1,1]
	v_pk_mov_b32 v[62:63], v[80:81], v[14:15] op_sel:[1,0]
	v_mov_b32_dpp v2, v85 row_shr:1 row_mask:0xf bank_mask:0xf
	v_mov_b32_e32 v107, v85
	v_pk_fma_f32 v[60:61], v[62:63], v[10:11], v[60:61]
	v_pk_mul_f32 v[62:63], v[106:107], v[2:3]
	v_mov_b32_dpp v35, v84 row_shl:1 row_mask:0xf bank_mask:0xf
	v_pk_fma_f32 v[62:63], v[84:85], v[28:29], v[62:63] op_sel_hi:[0,1,1]
	v_pk_mov_b32 v[68:69], v[84:85], v[122:123] op_sel:[1,0]
	v_mov_b32_e32 v92, v59
	v_pk_fma_f32 v[62:63], v[68:69], v[34:35], v[62:63]
	v_pk_add_f32 v[60:61], v[60:61], 0 op_sel_hi:[1,0]
	v_mov_b32_dpp v92, v117 row_shr:1 row_mask:0xf bank_mask:0xf
	v_mov_b32_e32 v97, v117
	v_accvgpr_read_b32 v87, a9
	v_pk_add_f32 v[60:61], v[60:61], v[62:63]
	v_pk_mul_f32 v[62:63], v[96:97], v[92:93]
	v_accvgpr_read_b32 v86, a8
	v_mov_b32_dpp v59, v116 row_shl:1 row_mask:0xf bank_mask:0xf
	v_pk_fma_f32 v[62:63], v[116:117], v[86:87], v[62:63] op_sel_hi:[0,1,1]
	v_pk_mov_b32 v[68:69], v[116:117], v[118:119] op_sel:[1,0]
	v_mov_b32_e32 v94, v57
	v_pk_fma_f32 v[62:63], v[68:69], v[58:59], v[62:63]
	s_mov_b64 s[0:1], 0x1820000
	v_pk_add_f32 v[60:61], v[60:61], v[62:63]
	v_mov_b32_dpp v94, v115 row_shr:1 row_mask:0xf bank_mask:0xf
	v_mov_b32_e32 v99, v115
	v_lshl_add_u64 v[62:63], v[54:55], 0, s[0:1]
	v_mov_b32_e32 v128, v60
	v_mov_b32_e32 v129, v61
	v_pk_mul_f32 v[60:61], v[98:99], v[94:95]
	v_mov_b32_e32 v102, v51
	v_mov_b32_dpp v57, v114 row_shl:1 row_mask:0xf bank_mask:0xf
	v_pk_fma_f32 v[60:61], v[114:115], v[40:41], v[60:61] op_sel_hi:[0,1,1]
	v_mov_b32_e32 v62, v115
	v_mov_b32_e32 v63, v15
	v_mov_b32_dpp v102, v113 row_shr:1 row_mask:0xf bank_mask:0xf
	v_mov_b32_e32 v105, v113
	v_accvgpr_read_b32 v89, a19
	v_pk_fma_f32 v[60:61], v[62:63], v[56:57], v[60:61]
	v_pk_mul_f32 v[62:63], v[104:105], v[102:103]
	v_accvgpr_read_b32 v88, a18
	v_mov_b32_dpp v51, v112 row_shl:1 row_mask:0xf bank_mask:0xf
	v_pk_fma_f32 v[62:63], v[112:113], v[88:89], v[62:63] op_sel_hi:[0,1,1]
	v_mov_b32_e32 v68, v113
	v_mov_b32_e32 v69, v123
	v_mov_b32_e32 v108, v49
	v_pk_fma_f32 v[62:63], v[68:69], v[50:51], v[62:63]
	v_pk_add_f32 v[60:61], v[60:61], 0 op_sel_hi:[1,0]
	v_mov_b32_dpp v108, v91 row_shr:1 row_mask:0xf bank_mask:0xf
	v_mov_b32_e32 v111, v91
	v_pk_add_f32 v[60:61], v[60:61], v[62:63]
	v_pk_mul_f32 v[62:63], v[110:111], v[108:109]
	v_mov_b32_dpp v49, v90 row_shl:1 row_mask:0xf bank_mask:0xf
	v_pk_fma_f32 v[62:63], v[90:91], v[4:5], v[62:63] op_sel_hi:[0,1,1]
	v_mov_b32_e32 v68, v91
	v_mov_b32_e32 v69, v119
	v_pk_fma_f32 v[62:63], v[68:69], v[48:49], v[62:63]
	s_mov_b64 s[0:1], 0x1830000
	v_pk_add_f32 v[60:61], v[60:61], v[62:63]
	v_lshl_add_u64 v[136:137], v[134:135], 0, s[0:1]
	s_nop 1
	s_mov_b64 vcc, s[28:29]
	s_nop 0
	v_cndmask_b32_dpp v130, v60, v128, vcc quad_perm:[1,0,3,2] row_mask:0xf bank_mask:0xf
	v_cndmask_b32_dpp v131, v61, v129, vcc quad_perm:[1,0,3,2] row_mask:0xf bank_mask:0xf
	s_mov_b64 vcc, s[30:31]
	s_nop 0
	v_cndmask_b32_dpp v132, v128, v60, vcc quad_perm:[1,0,3,2] row_mask:0xf bank_mask:0xf
	v_cndmask_b32_dpp v133, v129, v61, vcc quad_perm:[1,0,3,2] row_mask:0xf bank_mask:0xf
	global_store_dwordx4 v[136:137], v[130:133], off sc0 sc1 nt
	s_nop 1
	v_accvgpr_write_b32 a12, v28
	s_waitcnt vmcnt(8)
	v_accvgpr_write_b32 a13, v29
	v_mov_b64_e32 v[28:29], v[4:5]
	s_waitcnt lgkmcnt(0)
	s_barrier
	v_accvgpr_read_b32 v2, a6
	v_accvgpr_read_b32 v4, a7
	ds_read_b64 v[60:61], v2
	ds_read_b64 v[62:63], v2 offset:288
	ds_read_b64 v[68:69], v2 offset:576
	ds_read_b64 v[70:71], v2 offset:1728
	ds_read_b64 v[72:73], v2 offset:2016
	ds_read_b64 v[82:83], v2 offset:2304
	ds_read_b64 v[80:81], v2 offset:3456
	ds_read_b64 v[84:85], v2 offset:3744
	ds_read_b64 v[116:117], v2 offset:4032
	ds_read_b64 v[114:115], v2 offset:5184
	ds_read_b64 v[112:113], v2 offset:5472
	ds_read_b64 v[90:91], v2 offset:5760
	ds_read_b32 v43, v4
	ds_read_b32 v19, v4 offset:288
	ds_read_b32 v39, v4 offset:576
	ds_read_b32 v25, v4 offset:1728
	ds_read_b32 v7, v4 offset:2016
	ds_read_b32 v21, v4 offset:2304
	ds_read_b32 v11, v4 offset:3456
	ds_read_b32 v35, v4 offset:3744
	ds_read_b32 v59, v4 offset:4032
	ds_read_b32 v57, v4 offset:5184
	ds_read_b32 v51, v4 offset:5472
	ds_read_b32 v49, v4 offset:5760
	s_waitcnt lgkmcnt(0)
	v_accvgpr_read_b32 v8, a24
	v_mov_b32_e32 v46, v43
	v_mov_b32_e32 v65, v61
	v_mov_b32_e32 v26, v19
	v_mov_b32_dpp v46, v61 row_shr:1 row_mask:0xf bank_mask:0xf
	v_accvgpr_read_b32 v32, a32
	v_accvgpr_read_b32 v9, a25
	v_mov_b64_e32 v[124:125], v[40:41]
	v_pk_mul_f32 v[30:31], v[64:65], v[46:47]
	v_mov_b32_dpp v26, v63 row_shr:1 row_mask:0xf bank_mask:0xf
	v_mov_b32_e32 v33, v63
	v_accvgpr_read_b32 v4, a14
	v_accvgpr_read_b32 v41, a35
	v_mov_b32_e32 v44, v39
	v_pk_fma_f32 v[30:31], v[60:61], v[100:101], v[30:31] op_sel_hi:[0,1,1]
	v_mov_b32_dpp v43, v60 row_shl:1 row_mask:0xf bank_mask:0xf
	v_pk_mov_b32 v[46:47], v[60:61], v[8:9] op_sel:[1,0]
	v_pk_mul_f32 v[26:27], v[32:33], v[26:27]
	v_accvgpr_read_b32 v5, a15
	v_accvgpr_read_b32 v40, a34
	v_mov_b32_dpp v44, v69 row_shr:1 row_mask:0xf bank_mask:0xf
	v_mov_b32_e32 v17, v69
	v_accvgpr_read_b32 v0, a16
	v_pk_fma_f32 v[30:31], v[46:47], v[42:43], v[30:31]
	v_pk_fma_f32 v[26:27], v[62:63], v[4:5], v[26:27] op_sel_hi:[0,1,1]
	v_mov_b32_dpp v19, v62 row_shl:1 row_mask:0xf bank_mask:0xf
	v_pk_mov_b32 v[32:33], v[62:63], v[40:41] op_sel:[1,0]
	v_pk_mul_f32 v[16:17], v[16:17], v[44:45]
	v_accvgpr_read_b32 v1, a17
	v_pk_fma_f32 v[18:19], v[32:33], v[18:19], v[26:27]
	v_pk_add_f32 v[26:27], v[30:31], 0 op_sel_hi:[1,0]
	v_mov_b32_dpp v39, v68 row_shl:1 row_mask:0xf bank_mask:0xf
	v_pk_fma_f32 v[16:17], v[68:69], v[0:1], v[16:17] op_sel_hi:[0,1,1]
	v_pk_mov_b32 v[30:31], v[68:69], v[66:67] op_sel:[1,0]
	v_pk_add_f32 v[18:19], v[26:27], v[18:19]
	v_pk_fma_f32 v[16:17], v[30:31], v[38:39], v[16:17]
	v_mov_b32_e32 v36, v25
	s_mov_b64 s[0:1], 0x1c00000
	v_pk_add_f32 v[16:17], v[18:19], v[16:17]
	v_mov_b32_dpp v36, v71 row_shr:1 row_mask:0xf bank_mask:0xf
	v_mov_b32_e32 v127, v71
	v_accvgpr_read_b32 v0, a20
	v_lshl_add_u64 v[26:27], v[54:55], 0, s[0:1]
	v_mov_b32_e32 v128, v16
	v_mov_b32_e32 v129, v17
	v_mov_b32_e32 v12, v7
	v_pk_mul_f32 v[16:17], v[126:127], v[36:37]
	v_accvgpr_read_b32 v1, a21
	v_mov_b32_dpp v12, v73 row_shr:1 row_mask:0xf bank_mask:0xf
	v_pk_fma_f32 v[16:17], v[70:71], v[0:1], v[16:17] op_sel_hi:[0,1,1]
	v_mov_b32_e32 v75, v73
	v_accvgpr_read_b32 v0, a4
	v_mov_b32_e32 v78, v21
	v_pk_mul_f32 v[12:13], v[74:75], v[12:13]
	v_accvgpr_read_b32 v1, a5
	v_mov_b32_dpp v25, v70 row_shl:1 row_mask:0xf bank_mask:0xf
	v_mov_b32_dpp v7, v72 row_shl:1 row_mask:0xf bank_mask:0xf
	v_mov_b32_dpp v78, v83 row_shr:1 row_mask:0xf bank_mask:0xf
	v_mov_b32_e32 v8, v71
	v_pk_fma_f32 v[12:13], v[72:73], v[0:1], v[12:13] op_sel_hi:[0,1,1]
	v_mov_b32_e32 v5, v41
	v_mov_b32_e32 v4, v73
	v_mov_b32_e32 v53, v83
	v_pk_fma_f32 v[16:17], v[8:9], v[24:25], v[16:17]
	v_pk_fma_f32 v[6:7], v[4:5], v[6:7], v[12:13]
	v_pk_mul_f32 v[12:13], v[52:53], v[78:79]
	v_mov_b32_dpp v21, v82 row_shl:1 row_mask:0xf bank_mask:0xf
	v_pk_add_f32 v[16:17], v[16:17], 0 op_sel_hi:[1,0]
	v_pk_fma_f32 v[12:13], v[82:83], v[22:23], v[12:13] op_sel_hi:[0,1,1]
	v_mov_b32_e32 v66, v83
	v_pk_add_f32 v[6:7], v[16:17], v[6:7]
	v_pk_fma_f32 v[12:13], v[66:67], v[20:21], v[12:13]
	v_mov_b32_e32 v76, v11
	v_pk_add_f32 v[6:7], v[6:7], v[12:13]
	s_mov_b64 s[0:1], 0x1c10000
	v_mov_b32_dpp v76, v81 row_shr:1 row_mask:0xf bank_mask:0xf
	v_mov_b32_e32 v121, v81
	v_accvgpr_read_b32 v0, a36
	v_lshl_add_u64 v[136:137], v[134:135], 0, s[0:1]
	s_nop 1
	s_mov_b64 vcc, s[28:29]
	s_nop 0
	v_cndmask_b32_dpp v130, v6, v128, vcc quad_perm:[1,0,3,2] row_mask:0xf bank_mask:0xf
	v_cndmask_b32_dpp v131, v7, v129, vcc quad_perm:[1,0,3,2] row_mask:0xf bank_mask:0xf
	s_mov_b64 vcc, s[30:31]
	s_nop 0
	v_cndmask_b32_dpp v132, v128, v6, vcc quad_perm:[1,0,3,2] row_mask:0xf bank_mask:0xf
	v_cndmask_b32_dpp v133, v129, v7, vcc quad_perm:[1,0,3,2] row_mask:0xf bank_mask:0xf
	global_store_dwordx4 v[136:137], v[130:133], off sc0 sc1 nt
	s_nop 1
	v_mov_b32_e32 v2, v35
	v_pk_mul_f32 v[6:7], v[120:121], v[76:77]
	v_accvgpr_read_b32 v1, a37
	v_mov_b32_dpp v2, v85 row_shr:1 row_mask:0xf bank_mask:0xf
	v_pk_fma_f32 v[6:7], v[80:81], v[0:1], v[6:7] op_sel_hi:[0,1,1]
	v_mov_b32_e32 v107, v85
	v_accvgpr_read_b32 v0, a12
	v_mov_b32_e32 v92, v59
	v_pk_mul_f32 v[2:3], v[106:107], v[2:3]
	v_accvgpr_read_b32 v1, a13
	v_mov_b32_dpp v11, v80 row_shl:1 row_mask:0xf bank_mask:0xf
	v_mov_b32_dpp v35, v84 row_shl:1 row_mask:0xf bank_mask:0xf
	v_mov_b32_dpp v92, v117 row_shr:1 row_mask:0xf bank_mask:0xf
	v_pk_mov_b32 v[8:9], v[80:81], v[14:15] op_sel:[1,0]
	v_pk_fma_f32 v[2:3], v[84:85], v[0:1], v[2:3] op_sel_hi:[0,1,1]
	v_pk_mov_b32 v[4:5], v[84:85], v[122:123] op_sel:[1,0]
	v_mov_b32_e32 v97, v117
	v_pk_fma_f32 v[6:7], v[8:9], v[10:11], v[6:7]
	v_pk_fma_f32 v[0:1], v[4:5], v[34:35], v[2:3]
	v_pk_mul_f32 v[2:3], v[96:97], v[92:93]
	v_mov_b32_dpp v59, v116 row_shl:1 row_mask:0xf bank_mask:0xf
	v_pk_add_f32 v[6:7], v[6:7], 0 op_sel_hi:[1,0]
	v_pk_fma_f32 v[2:3], v[116:117], v[86:87], v[2:3] op_sel_hi:[0,1,1]
	v_pk_mov_b32 v[4:5], v[116:117], v[118:119] op_sel:[1,0]
	v_pk_add_f32 v[0:1], v[6:7], v[0:1]
	v_pk_fma_f32 v[2:3], v[4:5], v[58:59], v[2:3]
	v_mov_b32_e32 v94, v57
	v_pk_add_f32 v[0:1], v[0:1], v[2:3]
	s_mov_b64 s[0:1], 0x1c20000
	v_mov_b32_dpp v94, v115 row_shr:1 row_mask:0xf bank_mask:0xf
	v_mov_b32_e32 v102, v51
	v_mov_b32_e32 v99, v115
	v_lshl_add_u64 v[2:3], v[54:55], 0, s[0:1]
	v_mov_b32_e32 v128, v0
	v_mov_b32_e32 v129, v1
	v_mov_b32_dpp v102, v113 row_shr:1 row_mask:0xf bank_mask:0xf
	v_pk_mul_f32 v[0:1], v[98:99], v[94:95]
	v_mov_b32_e32 v105, v113
	v_mov_b32_dpp v57, v114 row_shl:1 row_mask:0xf bank_mask:0xf
	v_pk_fma_f32 v[0:1], v[114:115], v[124:125], v[0:1] op_sel_hi:[0,1,1]
	v_mov_b32_e32 v14, v115
	v_pk_mul_f32 v[2:3], v[104:105], v[102:103]
	v_mov_b32_dpp v51, v112 row_shl:1 row_mask:0xf bank_mask:0xf
	v_mov_b32_e32 v108, v49
	v_pk_fma_f32 v[0:1], v[14:15], v[56:57], v[0:1]
	v_pk_fma_f32 v[2:3], v[112:113], v[88:89], v[2:3] op_sel_hi:[0,1,1]
	v_mov_b32_e32 v122, v113
	v_mov_b32_dpp v108, v91 row_shr:1 row_mask:0xf bank_mask:0xf
	v_pk_add_f32 v[0:1], v[0:1], 0 op_sel_hi:[1,0]
	v_pk_fma_f32 v[2:3], v[122:123], v[50:51], v[2:3]
	v_mov_b32_e32 v111, v91
	v_pk_add_f32 v[0:1], v[0:1], v[2:3]
	v_pk_mul_f32 v[2:3], v[110:111], v[108:109]
	v_mov_b32_dpp v49, v90 row_shl:1 row_mask:0xf bank_mask:0xf
	v_pk_fma_f32 v[2:3], v[90:91], v[28:29], v[2:3] op_sel_hi:[0,1,1]
	v_mov_b32_e32 v118, v91
	v_pk_fma_f32 v[2:3], v[118:119], v[48:49], v[2:3]
	s_mov_b64 s[0:1], 0x1c30000
	v_pk_add_f32 v[0:1], v[0:1], v[2:3]
	v_lshl_add_u64 v[136:137], v[134:135], 0, s[0:1]
	s_nop 1
	s_mov_b64 vcc, s[28:29]
	s_nop 0
	v_cndmask_b32_dpp v130, v0, v128, vcc quad_perm:[1,0,3,2] row_mask:0xf bank_mask:0xf
	v_cndmask_b32_dpp v131, v1, v129, vcc quad_perm:[1,0,3,2] row_mask:0xf bank_mask:0xf
	s_mov_b64 vcc, s[30:31]
	s_nop 0
	v_cndmask_b32_dpp v132, v128, v0, vcc quad_perm:[1,0,3,2] row_mask:0xf bank_mask:0xf
	v_cndmask_b32_dpp v133, v129, v1, vcc quad_perm:[1,0,3,2] row_mask:0xf bank_mask:0xf
	global_store_dwordx4 v[136:137], v[130:133], off sc0 sc1 nt
	s_nop 1
	s_endpgm
